# kloop_mid_segment_setprio_flip_removed
# baseline (speedup 1.0000x reference)
.LBB0_253:
	v_add_u32_e32 v133, 0x10000, v131
	ds_read_b128 v[136:139], v133
	ds_read_b128 v[140:143], v133 offset:1024
	ds_read_b128 v[144:147], v133 offset:2048
	ds_read_b128 v[148:151], v133 offset:3072
	v_add_u32_e32 v133, 0x14000, v131
	ds_read_b128 v[152:155], v133
	ds_read_b128 v[156:159], v133 offset:1024
	ds_read_b128 v[160:163], v133 offset:2048
	ds_read_b128 v[164:167], v133 offset:3072
	s_cmp_eq_u32 s25, s61
	s_cselect_b64 s[66:67], -1, 0
	v_lshl_add_u64 v[192:193], s[0:1], 0, v[194:195]
	s_mov_b32 m0, s56
	v_lshl_add_u64 v[192:193], v[192:193], 0, s[26:27]
	v_mov_b32_e32 v133, v195
	ds_read_b128 v[168:171], v135
	ds_read_b128 v[172:175], v135 offset:1024
	ds_read_b128 v[176:179], v135 offset:2048
	ds_read_b128 v[180:183], v135 offset:3072
	ds_read_b128 v[184:187], v135 offset:4096
	ds_read_b128 v[188:191], v135 offset:5120
	ds_read_b128 v[196:199], v135 offset:6144
	ds_read_b128 v[200:203], v135 offset:7168
	global_load_lds_dwordx4 v[192:193], off
	v_lshl_add_u64 v[192:193], s[0:1], 0, v[132:133]
	v_lshl_add_u64 v[192:193], v[192:193], 0, s[26:27]
	s_mov_b32 m0, s57
	s_nop 0
	global_load_lds_dwordx4 v[192:193], off
	s_cmp_lg_u32 s100, 0
	s_waitcnt vmcnt(8)
	s_waitcnt lgkmcnt(0)
	s_barrier
	s_setprio 1
	s_waitcnt lgkmcnt(0)
	s_cbranch_scc1 .Lcz1_253
	v_mfma_f32_16x16x32_bf16 v[126:129], v[136:139], v[168:171], v[126:129]
	v_mfma_f32_16x16x32_bf16 v[122:125], v[144:147], v[168:171], v[122:125]
	v_mfma_f32_16x16x32_bf16 v[114:117], v[136:139], v[176:179], v[114:117]
	v_mfma_f32_16x16x32_bf16 v[110:113], v[144:147], v[176:179], v[110:113]
	v_mfma_f32_16x16x32_bf16 v[94:97], v[136:139], v[184:187], v[94:97]
	v_mfma_f32_16x16x32_bf16 v[90:93], v[144:147], v[184:187], v[90:93]
	v_mfma_f32_16x16x32_bf16 v[78:81], v[136:139], v[196:199], v[78:81]
	v_mfma_f32_16x16x32_bf16 v[74:77], v[144:147], v[196:199], v[74:77]
	v_mfma_f32_16x16x32_bf16 v[126:129], v[140:143], v[172:175], v[126:129]
	v_mfma_f32_16x16x32_bf16 v[122:125], v[148:151], v[172:175], v[122:125]
	v_mfma_f32_16x16x32_bf16 v[114:117], v[140:143], v[180:183], v[114:117]
	v_mfma_f32_16x16x32_bf16 v[110:113], v[148:151], v[180:183], v[110:113]
	v_mfma_f32_16x16x32_bf16 v[94:97], v[140:143], v[188:191], v[94:97]
	v_mfma_f32_16x16x32_bf16 v[90:93], v[148:151], v[188:191], v[90:93]
	v_mfma_f32_16x16x32_bf16 v[78:81], v[140:143], v[200:203], v[78:81]
	v_mfma_f32_16x16x32_bf16 v[74:77], v[148:151], v[200:203], v[74:77]
	v_mfma_f32_16x16x32_bf16 v[106:109], v[152:155], v[168:171], v[106:109]
	v_mfma_f32_16x16x32_bf16 v[118:121], v[160:163], v[168:171], v[118:121]
	v_mfma_f32_16x16x32_bf16 v[102:105], v[152:155], v[176:179], v[102:105]
	v_mfma_f32_16x16x32_bf16 v[98:101], v[160:163], v[176:179], v[98:101]
	v_mfma_f32_16x16x32_bf16 v[86:89], v[152:155], v[184:187], v[86:89]
	v_mfma_f32_16x16x32_bf16 v[82:85], v[160:163], v[184:187], v[82:85]
	v_mfma_f32_16x16x32_bf16 v[70:73], v[152:155], v[196:199], v[70:73]
	v_mfma_f32_16x16x32_bf16 v[66:69], v[160:163], v[196:199], v[66:69]
	v_mfma_f32_16x16x32_bf16 v[106:109], v[156:159], v[172:175], v[106:109]
	v_mfma_f32_16x16x32_bf16 v[118:121], v[164:167], v[172:175], v[118:121]
	v_mfma_f32_16x16x32_bf16 v[102:105], v[156:159], v[180:183], v[102:105]
	v_mfma_f32_16x16x32_bf16 v[98:101], v[164:167], v[180:183], v[98:101]
	v_mfma_f32_16x16x32_bf16 v[86:89], v[156:159], v[188:191], v[86:89]
	v_mfma_f32_16x16x32_bf16 v[82:85], v[164:167], v[188:191], v[82:85]
	v_mfma_f32_16x16x32_bf16 v[70:73], v[156:159], v[200:203], v[70:73]
	v_mfma_f32_16x16x32_bf16 v[66:69], v[164:167], v[200:203], v[66:69]
.Lcj1_253:
	s_setprio 0
	s_barrier
	s_and_b64 s[68:69], s[66:67], exec
	s_cselect_b32 s62, 0, s61
	s_and_b64 s[66:67], s[2:3], s[66:67]
	s_and_b64 s[66:67], s[66:67], exec
	s_cselect_b32 s5, s60, s5
	s_cselect_b32 s4, s21, s4
	s_cselect_b32 s1, s59, s1
	s_cselect_b32 s0, s23, s0
	s_lshl_b64 s[66:67], s[62:63], 7
	s_add_u32 s68, s4, s66
	s_addc_u32 s69, s5, s67
	s_mov_b32 m0, s41
	s_add_u32 s72, s4, 0x40000
	ds_read_b128 v[168:171], v135 offset:16384
	ds_read_b128 v[172:175], v135 offset:17408
	ds_read_b128 v[176:179], v135 offset:18432
	ds_read_b128 v[180:183], v135 offset:19456
	ds_read_b128 v[184:187], v135 offset:20480
	ds_read_b128 v[188:191], v135 offset:21504
	ds_read_b128 v[196:199], v135 offset:22528
	ds_read_b128 v[200:203], v135 offset:23552
	global_load_lds_dwordx4 v130, s[68:69]
	s_mov_b32 m0, s42
	s_addc_u32 s73, s5, 0
	global_load_lds_dwordx4 v134, s[68:69]
	s_add_u32 s68, s72, s66
	s_addc_u32 s69, s73, s67
	s_mov_b32 m0, s43
	s_add_u32 s66, s0, s66
	global_load_lds_dwordx4 v130, s[68:69]
	s_mov_b32 m0, s44
	s_addc_u32 s67, s1, s67
	global_load_lds_dwordx4 v134, s[68:69]
	s_mov_b32 m0, s40
	s_nop 0
	global_load_lds_dwordx4 v194, s[66:67]
	s_mov_b32 m0, s45
	s_nop 0
	global_load_lds_dwordx4 v132, s[66:67]
	s_cmp_lg_u32 s100, 0
	s_waitcnt vmcnt(8)
	s_waitcnt lgkmcnt(0)
	s_barrier
	s_setprio 1
	s_waitcnt lgkmcnt(0)
	s_cbranch_scc1 .Lcz2_253
	v_mfma_f32_16x16x32_bf16 v[62:65], v[136:139], v[168:171], v[62:65]
	v_mfma_f32_16x16x32_bf16 v[58:61], v[144:147], v[168:171], v[58:61]
	v_mfma_f32_16x16x32_bf16 v[46:49], v[136:139], v[176:179], v[46:49]
	v_mfma_f32_16x16x32_bf16 v[42:45], v[144:147], v[176:179], v[42:45]
	v_mfma_f32_16x16x32_bf16 v[30:33], v[136:139], v[184:187], v[30:33]
	v_mfma_f32_16x16x32_bf16 v[26:29], v[144:147], v[184:187], v[26:29]
	v_mfma_f32_16x16x32_bf16 v[14:17], v[136:139], v[196:199], v[14:17]
	v_mfma_f32_16x16x32_bf16 v[10:13], v[144:147], v[196:199], v[10:13]
	v_mfma_f32_16x16x32_bf16 v[62:65], v[140:143], v[172:175], v[62:65]
	v_mfma_f32_16x16x32_bf16 v[58:61], v[148:151], v[172:175], v[58:61]
	v_mfma_f32_16x16x32_bf16 v[46:49], v[140:143], v[180:183], v[46:49]
	v_mfma_f32_16x16x32_bf16 v[42:45], v[148:151], v[180:183], v[42:45]
	v_mfma_f32_16x16x32_bf16 v[30:33], v[140:143], v[188:191], v[30:33]
	v_mfma_f32_16x16x32_bf16 v[26:29], v[148:151], v[188:191], v[26:29]
	v_mfma_f32_16x16x32_bf16 v[14:17], v[140:143], v[200:203], v[14:17]
	v_mfma_f32_16x16x32_bf16 v[10:13], v[148:151], v[200:203], v[10:13]
	v_mfma_f32_16x16x32_bf16 v[54:57], v[152:155], v[168:171], v[54:57]
	v_mfma_f32_16x16x32_bf16 v[50:53], v[160:163], v[168:171], v[50:53]
	v_mfma_f32_16x16x32_bf16 v[38:41], v[152:155], v[176:179], v[38:41]
	v_mfma_f32_16x16x32_bf16 v[34:37], v[160:163], v[176:179], v[34:37]
	v_mfma_f32_16x16x32_bf16 v[22:25], v[152:155], v[184:187], v[22:25]
	v_mfma_f32_16x16x32_bf16 v[18:21], v[160:163], v[184:187], v[18:21]
	v_mfma_f32_16x16x32_bf16 v[6:9], v[152:155], v[196:199], v[6:9]
	v_mfma_f32_16x16x32_bf16 v[2:5], v[160:163], v[196:199], v[2:5]
	v_mfma_f32_16x16x32_bf16 v[54:57], v[156:159], v[172:175], v[54:57]
	v_mfma_f32_16x16x32_bf16 v[50:53], v[164:167], v[172:175], v[50:53]
	v_mfma_f32_16x16x32_bf16 v[38:41], v[156:159], v[180:183], v[38:41]
	v_mfma_f32_16x16x32_bf16 v[34:37], v[164:167], v[180:183], v[34:37]
	v_mfma_f32_16x16x32_bf16 v[22:25], v[156:159], v[188:191], v[22:25]
	v_mfma_f32_16x16x32_bf16 v[18:21], v[164:167], v[188:191], v[18:21]
	v_mfma_f32_16x16x32_bf16 v[6:9], v[156:159], v[200:203], v[6:9]
	v_mfma_f32_16x16x32_bf16 v[2:5], v[164:167], v[200:203], v[2:5]
.Lcj2_253:
	s_setprio 0
	s_barrier
	v_add_u32_e32 v133, 0x18000, v131
	ds_read_b128 v[136:139], v133
	ds_read_b128 v[140:143], v133 offset:1024
	ds_read_b128 v[144:147], v133 offset:2048
	ds_read_b128 v[148:151], v133 offset:3072
	v_add_u32_e32 v133, 0x1c000, v131
	ds_read_b128 v[152:155], v133
	ds_read_b128 v[156:159], v133 offset:1024
	ds_read_b128 v[160:163], v133 offset:2048
	ds_read_b128 v[164:167], v133 offset:3072
	s_add_u32 s66, s66, 0x40000
	s_addc_u32 s67, s67, 0
	s_mov_b32 m0, s46
	ds_read_b128 v[168:171], v135 offset:32768
	ds_read_b128 v[172:175], v135 offset:33792
	ds_read_b128 v[176:179], v135 offset:34816
	ds_read_b128 v[180:183], v135 offset:35840
	ds_read_b128 v[184:187], v135 offset:36864
	ds_read_b128 v[188:191], v135 offset:37888
	ds_read_b128 v[196:199], v135 offset:38912
	ds_read_b128 v[200:203], v135 offset:39936
	global_load_lds_dwordx4 v194, s[66:67]
	s_mov_b32 m0, s47
	s_nop 0
	global_load_lds_dwordx4 v132, s[66:67]
	s_waitcnt vmcnt(8)
	s_waitcnt lgkmcnt(0)
	s_barrier
	s_setprio 1
	s_waitcnt lgkmcnt(0)
	v_mfma_f32_16x16x32_bf16 v[126:129], v[136:139], v[168:171], v[126:129]
	v_mfma_f32_16x16x32_bf16 v[122:125], v[144:147], v[168:171], v[122:125]
	v_mfma_f32_16x16x32_bf16 v[114:117], v[136:139], v[176:179], v[114:117]
	v_mfma_f32_16x16x32_bf16 v[110:113], v[144:147], v[176:179], v[110:113]
	v_mfma_f32_16x16x32_bf16 v[94:97], v[136:139], v[184:187], v[94:97]
	v_mfma_f32_16x16x32_bf16 v[90:93], v[144:147], v[184:187], v[90:93]
	v_mfma_f32_16x16x32_bf16 v[78:81], v[136:139], v[196:199], v[78:81]
	v_mfma_f32_16x16x32_bf16 v[74:77], v[144:147], v[196:199], v[74:77]
	v_mfma_f32_16x16x32_bf16 v[126:129], v[140:143], v[172:175], v[126:129]
	v_mfma_f32_16x16x32_bf16 v[122:125], v[148:151], v[172:175], v[122:125]
	v_mfma_f32_16x16x32_bf16 v[114:117], v[140:143], v[180:183], v[114:117]
	v_mfma_f32_16x16x32_bf16 v[110:113], v[148:151], v[180:183], v[110:113]
	v_mfma_f32_16x16x32_bf16 v[94:97], v[140:143], v[188:191], v[94:97]
	v_mfma_f32_16x16x32_bf16 v[90:93], v[148:151], v[188:191], v[90:93]
	v_mfma_f32_16x16x32_bf16 v[78:81], v[140:143], v[200:203], v[78:81]
	v_mfma_f32_16x16x32_bf16 v[74:77], v[148:151], v[200:203], v[74:77]
	v_mfma_f32_16x16x32_bf16 v[106:109], v[152:155], v[168:171], v[106:109]
	v_mfma_f32_16x16x32_bf16 v[118:121], v[160:163], v[168:171], v[118:121]
	v_mfma_f32_16x16x32_bf16 v[102:105], v[152:155], v[176:179], v[102:105]
	v_mfma_f32_16x16x32_bf16 v[98:101], v[160:163], v[176:179], v[98:101]
	v_mfma_f32_16x16x32_bf16 v[86:89], v[152:155], v[184:187], v[86:89]
	v_mfma_f32_16x16x32_bf16 v[82:85], v[160:163], v[184:187], v[82:85]
	v_mfma_f32_16x16x32_bf16 v[70:73], v[152:155], v[196:199], v[70:73]
	v_mfma_f32_16x16x32_bf16 v[66:69], v[160:163], v[196:199], v[66:69]
	v_mfma_f32_16x16x32_bf16 v[106:109], v[156:159], v[172:175], v[106:109]
	v_mfma_f32_16x16x32_bf16 v[118:121], v[164:167], v[172:175], v[118:121]
	v_mfma_f32_16x16x32_bf16 v[102:105], v[156:159], v[180:183], v[102:105]
	v_mfma_f32_16x16x32_bf16 v[98:101], v[164:167], v[180:183], v[98:101]
	v_mfma_f32_16x16x32_bf16 v[86:89], v[156:159], v[188:191], v[86:89]
	v_mfma_f32_16x16x32_bf16 v[82:85], v[164:167], v[188:191], v[82:85]
	v_mfma_f32_16x16x32_bf16 v[70:73], v[156:159], v[200:203], v[70:73]
	v_mfma_f32_16x16x32_bf16 v[66:69], v[164:167], v[200:203], v[66:69]
	s_setprio 0
	s_barrier
	s_or_b32 s62, s62, 1
	s_lshl_b64 s[66:67], s[62:63], 7
	s_add_u32 s68, s4, s66
	s_mov_b32 m0, s48
	s_addc_u32 s69, s5, s67
	ds_read_b128 v[168:171], v135 offset:49152
	ds_read_b128 v[172:175], v135 offset:50176
	ds_read_b128 v[176:179], v135 offset:51200
	ds_read_b128 v[180:183], v135 offset:52224
	ds_read_b128 v[184:187], v135 offset:53248
	ds_read_b128 v[188:191], v135 offset:54272
	ds_read_b128 v[196:199], v135 offset:55296
	ds_read_b128 v[200:203], v135 offset:56320
	global_load_lds_dwordx4 v130, s[68:69]
	s_mov_b32 m0, s49
	s_nop 0
	global_load_lds_dwordx4 v134, s[68:69]
	s_add_u32 s68, s72, s66
	s_addc_u32 s69, s73, s67
	s_mov_b32 m0, s52
	s_add_u32 s66, s0, s66
	global_load_lds_dwordx4 v130, s[68:69]
	s_mov_b32 m0, s53
	s_addc_u32 s67, s1, s67
	global_load_lds_dwordx4 v134, s[68:69]
	s_mov_b32 m0, s50
	s_nop 0
	global_load_lds_dwordx4 v194, s[66:67]
	s_mov_b32 m0, s51
	s_nop 0
	global_load_lds_dwordx4 v132, s[66:67]
	s_waitcnt vmcnt(8)
	s_waitcnt lgkmcnt(0)
	s_barrier
	s_setprio 1
	s_waitcnt lgkmcnt(0)
	v_mfma_f32_16x16x32_bf16 v[62:65], v[136:139], v[168:171], v[62:65]
	v_mfma_f32_16x16x32_bf16 v[58:61], v[144:147], v[168:171], v[58:61]
	v_mfma_f32_16x16x32_bf16 v[46:49], v[136:139], v[176:179], v[46:49]
	v_mfma_f32_16x16x32_bf16 v[42:45], v[144:147], v[176:179], v[42:45]
	v_mfma_f32_16x16x32_bf16 v[30:33], v[136:139], v[184:187], v[30:33]
	v_mfma_f32_16x16x32_bf16 v[26:29], v[144:147], v[184:187], v[26:29]
	v_mfma_f32_16x16x32_bf16 v[14:17], v[136:139], v[196:199], v[14:17]
	v_mfma_f32_16x16x32_bf16 v[10:13], v[144:147], v[196:199], v[10:13]
	v_mfma_f32_16x16x32_bf16 v[62:65], v[140:143], v[172:175], v[62:65]
	v_mfma_f32_16x16x32_bf16 v[58:61], v[148:151], v[172:175], v[58:61]
	v_mfma_f32_16x16x32_bf16 v[46:49], v[140:143], v[180:183], v[46:49]
	v_mfma_f32_16x16x32_bf16 v[42:45], v[148:151], v[180:183], v[42:45]
	v_mfma_f32_16x16x32_bf16 v[30:33], v[140:143], v[188:191], v[30:33]
	v_mfma_f32_16x16x32_bf16 v[26:29], v[148:151], v[188:191], v[26:29]
	v_mfma_f32_16x16x32_bf16 v[14:17], v[140:143], v[200:203], v[14:17]
	v_mfma_f32_16x16x32_bf16 v[10:13], v[148:151], v[200:203], v[10:13]
	v_mfma_f32_16x16x32_bf16 v[54:57], v[152:155], v[168:171], v[54:57]
	v_mfma_f32_16x16x32_bf16 v[50:53], v[160:163], v[168:171], v[50:53]
	v_mfma_f32_16x16x32_bf16 v[38:41], v[152:155], v[176:179], v[38:41]
	v_mfma_f32_16x16x32_bf16 v[34:37], v[160:163], v[176:179], v[34:37]
	v_mfma_f32_16x16x32_bf16 v[22:25], v[152:155], v[184:187], v[22:25]
	v_mfma_f32_16x16x32_bf16 v[18:21], v[160:163], v[184:187], v[18:21]
	v_mfma_f32_16x16x32_bf16 v[6:9], v[152:155], v[196:199], v[6:9]
	v_mfma_f32_16x16x32_bf16 v[2:5], v[160:163], v[196:199], v[2:5]
	v_mfma_f32_16x16x32_bf16 v[54:57], v[156:159], v[172:175], v[54:57]
	v_mfma_f32_16x16x32_bf16 v[50:53], v[164:167], v[172:175], v[50:53]
	v_mfma_f32_16x16x32_bf16 v[38:41], v[156:159], v[180:183], v[38:41]
	v_mfma_f32_16x16x32_bf16 v[34:37], v[164:167], v[180:183], v[34:37]
	v_mfma_f32_16x16x32_bf16 v[22:25], v[156:159], v[188:191], v[22:25]
	v_mfma_f32_16x16x32_bf16 v[18:21], v[164:167], v[188:191], v[18:21]
	v_mfma_f32_16x16x32_bf16 v[6:9], v[156:159], v[200:203], v[6:9]
	v_mfma_f32_16x16x32_bf16 v[2:5], v[164:167], v[200:203], v[2:5]
	s_setprio 0
	s_barrier
	s_add_i32 s62, s61, 2
	s_add_u32 s26, s26, 0x100
	s_addc_u32 s27, s27, 0
	s_cmp_ge_i32 s61, s25
	s_mov_b32 s61, s62
	s_cbranch_scc0 .LBB0_253
	s_branch .Lcsk_253
.Lcz1_253:
	v_mfma_f32_16x16x32_bf16 v[126:129], v[136:139], v[168:171], 0
	v_mfma_f32_16x16x32_bf16 v[122:125], v[144:147], v[168:171], 0
	v_mfma_f32_16x16x32_bf16 v[114:117], v[136:139], v[176:179], 0
	v_mfma_f32_16x16x32_bf16 v[110:113], v[144:147], v[176:179], 0
	v_mfma_f32_16x16x32_bf16 v[94:97], v[136:139], v[184:187], 0
	v_mfma_f32_16x16x32_bf16 v[90:93], v[144:147], v[184:187], 0
	v_mfma_f32_16x16x32_bf16 v[78:81], v[136:139], v[196:199], 0
	v_mfma_f32_16x16x32_bf16 v[74:77], v[144:147], v[196:199], 0
	v_mfma_f32_16x16x32_bf16 v[126:129], v[140:143], v[172:175], v[126:129]
	v_mfma_f32_16x16x32_bf16 v[122:125], v[148:151], v[172:175], v[122:125]
	v_mfma_f32_16x16x32_bf16 v[114:117], v[140:143], v[180:183], v[114:117]
	v_mfma_f32_16x16x32_bf16 v[110:113], v[148:151], v[180:183], v[110:113]
	v_mfma_f32_16x16x32_bf16 v[94:97], v[140:143], v[188:191], v[94:97]
	v_mfma_f32_16x16x32_bf16 v[90:93], v[148:151], v[188:191], v[90:93]
	v_mfma_f32_16x16x32_bf16 v[78:81], v[140:143], v[200:203], v[78:81]
	v_mfma_f32_16x16x32_bf16 v[74:77], v[148:151], v[200:203], v[74:77]
	v_mfma_f32_16x16x32_bf16 v[106:109], v[152:155], v[168:171], 0
	v_mfma_f32_16x16x32_bf16 v[118:121], v[160:163], v[168:171], 0
	v_mfma_f32_16x16x32_bf16 v[102:105], v[152:155], v[176:179], 0
	v_mfma_f32_16x16x32_bf16 v[98:101], v[160:163], v[176:179], 0
	v_mfma_f32_16x16x32_bf16 v[86:89], v[152:155], v[184:187], 0
	v_mfma_f32_16x16x32_bf16 v[82:85], v[160:163], v[184:187], 0
	v_mfma_f32_16x16x32_bf16 v[70:73], v[152:155], v[196:199], 0
	v_mfma_f32_16x16x32_bf16 v[66:69], v[160:163], v[196:199], 0
	v_mfma_f32_16x16x32_bf16 v[106:109], v[156:159], v[172:175], v[106:109]
	v_mfma_f32_16x16x32_bf16 v[118:121], v[164:167], v[172:175], v[118:121]
	v_mfma_f32_16x16x32_bf16 v[102:105], v[156:159], v[180:183], v[102:105]
	v_mfma_f32_16x16x32_bf16 v[98:101], v[164:167], v[180:183], v[98:101]
	v_mfma_f32_16x16x32_bf16 v[86:89], v[156:159], v[188:191], v[86:89]
	v_mfma_f32_16x16x32_bf16 v[82:85], v[164:167], v[188:191], v[82:85]
	v_mfma_f32_16x16x32_bf16 v[70:73], v[156:159], v[200:203], v[70:73]
	v_mfma_f32_16x16x32_bf16 v[66:69], v[164:167], v[200:203], v[66:69]
	s_branch .Lcj1_253
.Lcz2_253:
	v_mfma_f32_16x16x32_bf16 v[62:65], v[136:139], v[168:171], 0
	v_mfma_f32_16x16x32_bf16 v[58:61], v[144:147], v[168:171], 0
	v_mfma_f32_16x16x32_bf16 v[46:49], v[136:139], v[176:179], 0
	v_mfma_f32_16x16x32_bf16 v[42:45], v[144:147], v[176:179], 0
	v_mfma_f32_16x16x32_bf16 v[30:33], v[136:139], v[184:187], 0
	v_mfma_f32_16x16x32_bf16 v[26:29], v[144:147], v[184:187], 0
	v_mfma_f32_16x16x32_bf16 v[14:17], v[136:139], v[196:199], 0
	v_mfma_f32_16x16x32_bf16 v[10:13], v[144:147], v[196:199], 0
	v_mfma_f32_16x16x32_bf16 v[62:65], v[140:143], v[172:175], v[62:65]
	v_mfma_f32_16x16x32_bf16 v[58:61], v[148:151], v[172:175], v[58:61]
	v_mfma_f32_16x16x32_bf16 v[46:49], v[140:143], v[180:183], v[46:49]
	v_mfma_f32_16x16x32_bf16 v[42:45], v[148:151], v[180:183], v[42:45]
	v_mfma_f32_16x16x32_bf16 v[30:33], v[140:143], v[188:191], v[30:33]
	v_mfma_f32_16x16x32_bf16 v[26:29], v[148:151], v[188:191], v[26:29]
	v_mfma_f32_16x16x32_bf16 v[14:17], v[140:143], v[200:203], v[14:17]
	v_mfma_f32_16x16x32_bf16 v[10:13], v[148:151], v[200:203], v[10:13]
	v_mfma_f32_16x16x32_bf16 v[54:57], v[152:155], v[168:171], 0
	v_mfma_f32_16x16x32_bf16 v[50:53], v[160:163], v[168:171], 0
	v_mfma_f32_16x16x32_bf16 v[38:41], v[152:155], v[176:179], 0
	v_mfma_f32_16x16x32_bf16 v[34:37], v[160:163], v[176:179], 0
	v_mfma_f32_16x16x32_bf16 v[22:25], v[152:155], v[184:187], 0
	v_mfma_f32_16x16x32_bf16 v[18:21], v[160:163], v[184:187], 0
	v_mfma_f32_16x16x32_bf16 v[6:9], v[152:155], v[196:199], 0
	v_mfma_f32_16x16x32_bf16 v[2:5], v[160:163], v[196:199], 0
	v_mfma_f32_16x16x32_bf16 v[54:57], v[156:159], v[172:175], v[54:57]
	v_mfma_f32_16x16x32_bf16 v[50:53], v[164:167], v[172:175], v[50:53]
	v_mfma_f32_16x16x32_bf16 v[38:41], v[156:159], v[180:183], v[38:41]
	v_mfma_f32_16x16x32_bf16 v[34:37], v[164:167], v[180:183], v[34:37]
	v_mfma_f32_16x16x32_bf16 v[22:25], v[156:159], v[188:191], v[22:25]
	v_mfma_f32_16x16x32_bf16 v[18:21], v[164:167], v[188:191], v[18:21]
	v_mfma_f32_16x16x32_bf16 v[6:9], v[156:159], v[200:203], v[6:9]
	v_mfma_f32_16x16x32_bf16 v[2:5], v[164:167], v[200:203], v[2:5]
	s_mov_b32 s100, 0
	s_branch .Lcj2_253

.LBB0_287:
	v_add_u32_e32 v130, 0x10000, v165
	v_add_u32_e32 v142, 0x14000, v165
	ds_read_b128 v[146:149], v130
	ds_read_b128 v[150:153], v130 offset:1024
	ds_read_b128 v[154:157], v130 offset:2048
	ds_read_b128 v[158:161], v130 offset:3072
	ds_read_b128 v[130:133], v142
	ds_read_b128 v[134:137], v142 offset:1024
	ds_read_b128 v[138:141], v142 offset:2048
	ds_read_b128 v[142:145], v142 offset:3072
	s_add_i32 m0, s13, 0xc000
	s_add_i32 s26, s13, 0xe000
	s_cmp_lg_u32 s55, s56
	s_cselect_b64 s[58:59], -1, 0
	v_lshl_add_u64 v[204:205], s[10:11], 0, v[194:195]
	v_lshl_add_u64 v[204:205], v[204:205], 0, s[24:25]
	v_mov_b32_e32 v163, v195
	ds_read_b128 v[174:177], v167
	ds_read_b128 v[178:181], v167 offset:1024
	ds_read_b128 v[182:185], v167 offset:2048
	ds_read_b128 v[186:189], v167 offset:3072
	ds_read_b128 v[190:193], v167 offset:4096
	ds_read_b128 v[196:199], v167 offset:5120
	ds_read_b128 v[200:203], v167 offset:6144
	ds_read_b128 v[216:219], v167 offset:7168
	global_load_lds_dwordx4 v[204:205], off
	v_lshl_add_u64 v[204:205], s[10:11], 0, v[162:163]
	v_lshl_add_u64 v[204:205], v[204:205], 0, s[24:25]
	s_mov_b32 m0, s26
	s_nop 0
	global_load_lds_dwordx4 v[204:205], off
	s_cmp_lg_u32 s100, 0
	s_waitcnt vmcnt(8)
	s_waitcnt lgkmcnt(0)
	s_barrier
	s_setprio 1
	s_waitcnt lgkmcnt(0)
	s_cbranch_scc1 .Lcz1_287
	v_mfma_f32_16x16x32_bf16 v[126:129], v[146:149], v[174:177], v[126:129]
	v_mfma_f32_16x16x32_bf16 v[122:125], v[154:157], v[174:177], v[122:125]
	v_mfma_f32_16x16x32_bf16 v[110:113], v[146:149], v[182:185], v[110:113]
	v_mfma_f32_16x16x32_bf16 v[106:109], v[154:157], v[182:185], v[106:109]
	v_mfma_f32_16x16x32_bf16 v[94:97], v[146:149], v[190:193], v[94:97]
	v_mfma_f32_16x16x32_bf16 v[90:93], v[154:157], v[190:193], v[90:93]
	v_mfma_f32_16x16x32_bf16 v[78:81], v[146:149], v[200:203], v[78:81]
	v_mfma_f32_16x16x32_bf16 v[74:77], v[154:157], v[200:203], v[74:77]
	v_mfma_f32_16x16x32_bf16 v[126:129], v[150:153], v[178:181], v[126:129]
	v_mfma_f32_16x16x32_bf16 v[122:125], v[158:161], v[178:181], v[122:125]
	v_mfma_f32_16x16x32_bf16 v[110:113], v[150:153], v[186:189], v[110:113]
	v_mfma_f32_16x16x32_bf16 v[106:109], v[158:161], v[186:189], v[106:109]
	v_mfma_f32_16x16x32_bf16 v[94:97], v[150:153], v[196:199], v[94:97]
	v_mfma_f32_16x16x32_bf16 v[90:93], v[158:161], v[196:199], v[90:93]
	v_mfma_f32_16x16x32_bf16 v[78:81], v[150:153], v[216:219], v[78:81]
	v_mfma_f32_16x16x32_bf16 v[74:77], v[158:161], v[216:219], v[74:77]
	v_mfma_f32_16x16x32_bf16 v[118:121], v[130:133], v[174:177], v[118:121]
	v_mfma_f32_16x16x32_bf16 v[114:117], v[138:141], v[174:177], v[114:117]
	v_mfma_f32_16x16x32_bf16 v[102:105], v[130:133], v[182:185], v[102:105]
	v_mfma_f32_16x16x32_bf16 v[98:101], v[138:141], v[182:185], v[98:101]
	v_mfma_f32_16x16x32_bf16 v[86:89], v[130:133], v[190:193], v[86:89]
	v_mfma_f32_16x16x32_bf16 v[82:85], v[138:141], v[190:193], v[82:85]
	v_mfma_f32_16x16x32_bf16 v[70:73], v[130:133], v[200:203], v[70:73]
	v_mfma_f32_16x16x32_bf16 v[66:69], v[138:141], v[200:203], v[66:69]
	v_mfma_f32_16x16x32_bf16 v[118:121], v[134:137], v[178:181], v[118:121]
	v_mfma_f32_16x16x32_bf16 v[114:117], v[142:145], v[178:181], v[114:117]
	v_mfma_f32_16x16x32_bf16 v[102:105], v[134:137], v[186:189], v[102:105]
	v_mfma_f32_16x16x32_bf16 v[98:101], v[142:145], v[186:189], v[98:101]
	v_mfma_f32_16x16x32_bf16 v[86:89], v[134:137], v[196:199], v[86:89]
	v_mfma_f32_16x16x32_bf16 v[82:85], v[142:145], v[196:199], v[82:85]
	v_mfma_f32_16x16x32_bf16 v[70:73], v[134:137], v[216:219], v[70:73]
	v_mfma_f32_16x16x32_bf16 v[66:69], v[142:145], v[216:219], v[66:69]

.LBB0_289:
	s_ashr_i32 s27, s26, 31
	s_lshl_b64 s[26:27], s[26:27], 7
	s_add_u32 s58, s18, s26
	s_mov_b32 m0, s38
	s_addc_u32 s59, s19, s27
	ds_read_b128 v[174:177], v167 offset:16384
	ds_read_b128 v[178:181], v167 offset:17408
	ds_read_b128 v[182:185], v167 offset:18432
	ds_read_b128 v[186:189], v167 offset:19456
	ds_read_b128 v[190:193], v167 offset:20480
	ds_read_b128 v[196:199], v167 offset:21504
	ds_read_b128 v[200:203], v167 offset:22528
	ds_read_b128 v[216:219], v167 offset:23552
	global_load_lds_dwordx4 v164, s[58:59]
	s_mov_b32 m0, s39
	s_nop 0
	global_load_lds_dwordx4 v168, s[58:59]
	s_mov_b32 m0, s40
	s_nop 0
	global_load_lds_dwordx4 v166, s[58:59]
	s_mov_b32 m0, s41
	s_nop 0
	global_load_lds_dwordx4 v170, s[58:59]
	s_add_u32 s58, s10, s26
	s_addc_u32 s59, s11, s27
	v_lshl_add_u64 v[204:205], s[58:59], 0, v[194:195]
	s_mov_b32 m0, s13
	s_nop 0
	global_load_lds_dwordx4 v[204:205], off
	v_lshl_add_u64 v[204:205], s[58:59], 0, v[162:163]
	s_mov_b32 m0, s42
	s_nop 0
	global_load_lds_dwordx4 v[204:205], off
	s_cmp_lg_u32 s100, 0
	s_waitcnt vmcnt(8)
	s_waitcnt lgkmcnt(0)
	s_barrier
	s_setprio 1
	s_waitcnt lgkmcnt(0)
	s_cbranch_scc1 .Lcz2_287
	v_mfma_f32_16x16x32_bf16 v[62:65], v[146:149], v[174:177], v[62:65]
	v_mfma_f32_16x16x32_bf16 v[58:61], v[154:157], v[174:177], v[58:61]
	v_mfma_f32_16x16x32_bf16 v[46:49], v[146:149], v[182:185], v[46:49]
	v_mfma_f32_16x16x32_bf16 v[42:45], v[154:157], v[182:185], v[42:45]
	v_mfma_f32_16x16x32_bf16 v[30:33], v[146:149], v[190:193], v[30:33]
	v_mfma_f32_16x16x32_bf16 v[26:29], v[154:157], v[190:193], v[26:29]
	v_mfma_f32_16x16x32_bf16 v[14:17], v[146:149], v[200:203], v[14:17]
	v_mfma_f32_16x16x32_bf16 v[10:13], v[154:157], v[200:203], v[10:13]
	v_mfma_f32_16x16x32_bf16 v[62:65], v[150:153], v[178:181], v[62:65]
	v_mfma_f32_16x16x32_bf16 v[58:61], v[158:161], v[178:181], v[58:61]
	v_mfma_f32_16x16x32_bf16 v[46:49], v[150:153], v[186:189], v[46:49]
	v_mfma_f32_16x16x32_bf16 v[42:45], v[158:161], v[186:189], v[42:45]
	v_mfma_f32_16x16x32_bf16 v[30:33], v[150:153], v[196:199], v[30:33]
	v_mfma_f32_16x16x32_bf16 v[26:29], v[158:161], v[196:199], v[26:29]
	v_mfma_f32_16x16x32_bf16 v[14:17], v[150:153], v[216:219], v[14:17]
	v_mfma_f32_16x16x32_bf16 v[10:13], v[158:161], v[216:219], v[10:13]
	v_mfma_f32_16x16x32_bf16 v[54:57], v[130:133], v[174:177], v[54:57]
	v_mfma_f32_16x16x32_bf16 v[50:53], v[138:141], v[174:177], v[50:53]
	v_mfma_f32_16x16x32_bf16 v[38:41], v[130:133], v[182:185], v[38:41]
	v_mfma_f32_16x16x32_bf16 v[34:37], v[138:141], v[182:185], v[34:37]
	v_mfma_f32_16x16x32_bf16 v[22:25], v[130:133], v[190:193], v[22:25]
	v_mfma_f32_16x16x32_bf16 v[18:21], v[138:141], v[190:193], v[18:21]
	v_mfma_f32_16x16x32_bf16 v[6:9], v[130:133], v[200:203], v[6:9]
	v_mfma_f32_16x16x32_bf16 v[2:5], v[138:141], v[200:203], v[2:5]
	v_mfma_f32_16x16x32_bf16 v[54:57], v[134:137], v[178:181], v[54:57]
	v_mfma_f32_16x16x32_bf16 v[50:53], v[142:145], v[178:181], v[50:53]
	v_mfma_f32_16x16x32_bf16 v[38:41], v[134:137], v[186:189], v[38:41]
	v_mfma_f32_16x16x32_bf16 v[34:37], v[142:145], v[186:189], v[34:37]
	v_mfma_f32_16x16x32_bf16 v[22:25], v[134:137], v[196:199], v[22:25]
	v_mfma_f32_16x16x32_bf16 v[18:21], v[142:145], v[196:199], v[18:21]
	v_mfma_f32_16x16x32_bf16 v[6:9], v[134:137], v[216:219], v[6:9]
	v_mfma_f32_16x16x32_bf16 v[2:5], v[142:145], v[216:219], v[2:5]
.Lcj2_287:
	s_setprio 0
	s_barrier
	v_add_u32_e32 v142, 0x18000, v165
	v_add_u32_e32 v158, 0x1c000, v165
	ds_read_b128 v[130:133], v142
	ds_read_b128 v[134:137], v142 offset:1024
	ds_read_b128 v[138:141], v142 offset:2048
	ds_read_b128 v[142:145], v142 offset:3072
	ds_read_b128 v[146:149], v158
	ds_read_b128 v[150:153], v158 offset:1024
	ds_read_b128 v[154:157], v158 offset:2048
	ds_read_b128 v[158:161], v158 offset:3072
	s_add_u32 s58, s58, 0x40000
	s_addc_u32 s59, s59, 0
	s_mov_b32 m0, s43
	v_lshl_add_u64 v[204:205], s[58:59], 0, v[194:195]
	ds_read_b128 v[174:177], v167 offset:32768
	ds_read_b128 v[178:181], v167 offset:33792
	ds_read_b128 v[182:185], v167 offset:34816
	ds_read_b128 v[186:189], v167 offset:35840
	ds_read_b128 v[190:193], v167 offset:36864
	ds_read_b128 v[196:199], v167 offset:37888
	ds_read_b128 v[200:203], v167 offset:38912
	ds_read_b128 v[216:219], v167 offset:39936
	global_load_lds_dwordx4 v[204:205], off
	v_lshl_add_u64 v[204:205], s[58:59], 0, v[162:163]
	s_mov_b32 m0, s44
	s_nop 0
	global_load_lds_dwordx4 v[204:205], off
	s_waitcnt vmcnt(8)
	s_waitcnt lgkmcnt(0)
	s_barrier
	s_setprio 1
	s_waitcnt lgkmcnt(0)
	v_mfma_f32_16x16x32_bf16 v[126:129], v[130:133], v[174:177], v[126:129]
	v_mfma_f32_16x16x32_bf16 v[122:125], v[138:141], v[174:177], v[122:125]
	v_mfma_f32_16x16x32_bf16 v[110:113], v[130:133], v[182:185], v[110:113]
	v_mfma_f32_16x16x32_bf16 v[106:109], v[138:141], v[182:185], v[106:109]
	v_mfma_f32_16x16x32_bf16 v[94:97], v[130:133], v[190:193], v[94:97]
	v_mfma_f32_16x16x32_bf16 v[90:93], v[138:141], v[190:193], v[90:93]
	v_mfma_f32_16x16x32_bf16 v[78:81], v[130:133], v[200:203], v[78:81]
	v_mfma_f32_16x16x32_bf16 v[74:77], v[138:141], v[200:203], v[74:77]
	v_mfma_f32_16x16x32_bf16 v[126:129], v[134:137], v[178:181], v[126:129]
	v_mfma_f32_16x16x32_bf16 v[122:125], v[142:145], v[178:181], v[122:125]
	v_mfma_f32_16x16x32_bf16 v[110:113], v[134:137], v[186:189], v[110:113]
	v_mfma_f32_16x16x32_bf16 v[106:109], v[142:145], v[186:189], v[106:109]
	v_mfma_f32_16x16x32_bf16 v[94:97], v[134:137], v[196:199], v[94:97]
	v_mfma_f32_16x16x32_bf16 v[90:93], v[142:145], v[196:199], v[90:93]
	v_mfma_f32_16x16x32_bf16 v[78:81], v[134:137], v[216:219], v[78:81]
	v_mfma_f32_16x16x32_bf16 v[74:77], v[142:145], v[216:219], v[74:77]
	v_mfma_f32_16x16x32_bf16 v[118:121], v[146:149], v[174:177], v[118:121]
	v_mfma_f32_16x16x32_bf16 v[114:117], v[154:157], v[174:177], v[114:117]
	v_mfma_f32_16x16x32_bf16 v[102:105], v[146:149], v[182:185], v[102:105]
	v_mfma_f32_16x16x32_bf16 v[98:101], v[154:157], v[182:185], v[98:101]
	v_mfma_f32_16x16x32_bf16 v[86:89], v[146:149], v[190:193], v[86:89]
	v_mfma_f32_16x16x32_bf16 v[82:85], v[154:157], v[190:193], v[82:85]
	v_mfma_f32_16x16x32_bf16 v[70:73], v[146:149], v[200:203], v[70:73]
	v_mfma_f32_16x16x32_bf16 v[66:69], v[154:157], v[200:203], v[66:69]
	v_mfma_f32_16x16x32_bf16 v[118:121], v[150:153], v[178:181], v[118:121]
	v_mfma_f32_16x16x32_bf16 v[114:117], v[158:161], v[178:181], v[114:117]
	v_mfma_f32_16x16x32_bf16 v[102:105], v[150:153], v[186:189], v[102:105]
	v_mfma_f32_16x16x32_bf16 v[98:101], v[158:161], v[186:189], v[98:101]
	v_mfma_f32_16x16x32_bf16 v[86:89], v[150:153], v[196:199], v[86:89]
	v_mfma_f32_16x16x32_bf16 v[82:85], v[158:161], v[196:199], v[82:85]
	v_mfma_f32_16x16x32_bf16 v[70:73], v[150:153], v[216:219], v[70:73]
	v_mfma_f32_16x16x32_bf16 v[66:69], v[158:161], v[216:219], v[66:69]
	s_setprio 0
	s_barrier
	s_add_u32 s57, s26, 0x80
	s_addc_u32 s58, s27, 0
	s_add_u32 s26, s18, s57
	s_mov_b32 m0, s46
	s_addc_u32 s27, s19, s58
	ds_read_b128 v[174:177], v167 offset:49152
	ds_read_b128 v[178:181], v167 offset:50176
	ds_read_b128 v[182:185], v167 offset:51200
	ds_read_b128 v[186:189], v167 offset:52224
	ds_read_b128 v[190:193], v167 offset:53248
	ds_read_b128 v[196:199], v167 offset:54272
	ds_read_b128 v[200:203], v167 offset:55296
	ds_read_b128 v[216:219], v167 offset:56320
	global_load_lds_dwordx4 v164, s[26:27]
	s_mov_b32 m0, s47
	s_nop 0
	global_load_lds_dwordx4 v168, s[26:27]
	s_mov_b32 m0, s50
	s_nop 0
	global_load_lds_dwordx4 v166, s[26:27]
	s_mov_b32 m0, s51
	s_nop 0
	global_load_lds_dwordx4 v170, s[26:27]
	s_add_u32 s26, s10, s57
	s_addc_u32 s27, s11, s58
	v_lshl_add_u64 v[204:205], s[26:27], 0, v[194:195]
	s_mov_b32 m0, s48
	s_nop 0
	global_load_lds_dwordx4 v[204:205], off
	v_lshl_add_u64 v[204:205], s[26:27], 0, v[162:163]
	s_mov_b32 m0, s49
	s_nop 0
	global_load_lds_dwordx4 v[204:205], off
	s_waitcnt vmcnt(8)
	s_waitcnt lgkmcnt(0)
	s_barrier
	s_setprio 1
	s_waitcnt lgkmcnt(0)
	v_mfma_f32_16x16x32_bf16 v[62:65], v[130:133], v[174:177], v[62:65]
	v_mfma_f32_16x16x32_bf16 v[58:61], v[138:141], v[174:177], v[58:61]
	v_mfma_f32_16x16x32_bf16 v[46:49], v[130:133], v[182:185], v[46:49]
	v_mfma_f32_16x16x32_bf16 v[42:45], v[138:141], v[182:185], v[42:45]
	v_mfma_f32_16x16x32_bf16 v[30:33], v[130:133], v[190:193], v[30:33]
	v_mfma_f32_16x16x32_bf16 v[26:29], v[138:141], v[190:193], v[26:29]
	v_mfma_f32_16x16x32_bf16 v[14:17], v[130:133], v[200:203], v[14:17]
	v_mfma_f32_16x16x32_bf16 v[10:13], v[138:141], v[200:203], v[10:13]
	v_mfma_f32_16x16x32_bf16 v[62:65], v[134:137], v[178:181], v[62:65]
	v_mfma_f32_16x16x32_bf16 v[58:61], v[142:145], v[178:181], v[58:61]
	v_mfma_f32_16x16x32_bf16 v[46:49], v[134:137], v[186:189], v[46:49]
	v_mfma_f32_16x16x32_bf16 v[42:45], v[142:145], v[186:189], v[42:45]
	v_mfma_f32_16x16x32_bf16 v[30:33], v[134:137], v[196:199], v[30:33]
	v_mfma_f32_16x16x32_bf16 v[26:29], v[142:145], v[196:199], v[26:29]
	v_mfma_f32_16x16x32_bf16 v[14:17], v[134:137], v[216:219], v[14:17]
	v_mfma_f32_16x16x32_bf16 v[10:13], v[142:145], v[216:219], v[10:13]
	v_mfma_f32_16x16x32_bf16 v[54:57], v[146:149], v[174:177], v[54:57]
	v_mfma_f32_16x16x32_bf16 v[50:53], v[154:157], v[174:177], v[50:53]
	v_mfma_f32_16x16x32_bf16 v[38:41], v[146:149], v[182:185], v[38:41]
	v_mfma_f32_16x16x32_bf16 v[34:37], v[154:157], v[182:185], v[34:37]
	v_mfma_f32_16x16x32_bf16 v[22:25], v[146:149], v[190:193], v[22:25]
	v_mfma_f32_16x16x32_bf16 v[18:21], v[154:157], v[190:193], v[18:21]
	v_mfma_f32_16x16x32_bf16 v[6:9], v[146:149], v[200:203], v[6:9]
	v_mfma_f32_16x16x32_bf16 v[2:5], v[154:157], v[200:203], v[2:5]
	v_mfma_f32_16x16x32_bf16 v[54:57], v[150:153], v[178:181], v[54:57]
	v_mfma_f32_16x16x32_bf16 v[50:53], v[158:161], v[178:181], v[50:53]
	v_mfma_f32_16x16x32_bf16 v[38:41], v[150:153], v[186:189], v[38:41]
	v_mfma_f32_16x16x32_bf16 v[34:37], v[158:161], v[186:189], v[34:37]
	v_mfma_f32_16x16x32_bf16 v[22:25], v[150:153], v[196:199], v[22:25]
	v_mfma_f32_16x16x32_bf16 v[18:21], v[158:161], v[196:199], v[18:21]
	v_mfma_f32_16x16x32_bf16 v[6:9], v[150:153], v[216:219], v[6:9]
	v_mfma_f32_16x16x32_bf16 v[2:5], v[158:161], v[216:219], v[2:5]
	s_setprio 0
	s_barrier
	s_add_i32 s26, s56, 2
	s_add_u32 s24, s24, 0x100
	s_addc_u32 s25, s25, 0
	s_cmp_ge_i32 s56, s55
	s_cbranch_scc1 .LBB0_292
	s_mov_b32 s56, s26
	s_branch .LBB0_287
.Lcz1_287:
	v_mfma_f32_16x16x32_bf16 v[126:129], v[146:149], v[174:177], 0
	v_mfma_f32_16x16x32_bf16 v[122:125], v[154:157], v[174:177], 0
	v_mfma_f32_16x16x32_bf16 v[110:113], v[146:149], v[182:185], 0
	v_mfma_f32_16x16x32_bf16 v[106:109], v[154:157], v[182:185], 0
	v_mfma_f32_16x16x32_bf16 v[94:97], v[146:149], v[190:193], 0
	v_mfma_f32_16x16x32_bf16 v[90:93], v[154:157], v[190:193], 0
	v_mfma_f32_16x16x32_bf16 v[78:81], v[146:149], v[200:203], 0
	v_mfma_f32_16x16x32_bf16 v[74:77], v[154:157], v[200:203], 0
	v_mfma_f32_16x16x32_bf16 v[126:129], v[150:153], v[178:181], v[126:129]
	v_mfma_f32_16x16x32_bf16 v[122:125], v[158:161], v[178:181], v[122:125]
	v_mfma_f32_16x16x32_bf16 v[110:113], v[150:153], v[186:189], v[110:113]
	v_mfma_f32_16x16x32_bf16 v[106:109], v[158:161], v[186:189], v[106:109]
	v_mfma_f32_16x16x32_bf16 v[94:97], v[150:153], v[196:199], v[94:97]
	v_mfma_f32_16x16x32_bf16 v[90:93], v[158:161], v[196:199], v[90:93]
	v_mfma_f32_16x16x32_bf16 v[78:81], v[150:153], v[216:219], v[78:81]
	v_mfma_f32_16x16x32_bf16 v[74:77], v[158:161], v[216:219], v[74:77]
	v_mfma_f32_16x16x32_bf16 v[118:121], v[130:133], v[174:177], 0
	v_mfma_f32_16x16x32_bf16 v[114:117], v[138:141], v[174:177], 0
	v_mfma_f32_16x16x32_bf16 v[102:105], v[130:133], v[182:185], 0
	v_mfma_f32_16x16x32_bf16 v[98:101], v[138:141], v[182:185], 0
	v_mfma_f32_16x16x32_bf16 v[86:89], v[130:133], v[190:193], 0
	v_mfma_f32_16x16x32_bf16 v[82:85], v[138:141], v[190:193], 0
	v_mfma_f32_16x16x32_bf16 v[70:73], v[130:133], v[200:203], 0
	v_mfma_f32_16x16x32_bf16 v[66:69], v[138:141], v[200:203], 0
	v_mfma_f32_16x16x32_bf16 v[118:121], v[134:137], v[178:181], v[118:121]
	v_mfma_f32_16x16x32_bf16 v[114:117], v[142:145], v[178:181], v[114:117]
	v_mfma_f32_16x16x32_bf16 v[102:105], v[134:137], v[186:189], v[102:105]
	v_mfma_f32_16x16x32_bf16 v[98:101], v[142:145], v[186:189], v[98:101]
	v_mfma_f32_16x16x32_bf16 v[86:89], v[134:137], v[196:199], v[86:89]
	v_mfma_f32_16x16x32_bf16 v[82:85], v[142:145], v[196:199], v[82:85]
	v_mfma_f32_16x16x32_bf16 v[70:73], v[134:137], v[216:219], v[70:73]
	v_mfma_f32_16x16x32_bf16 v[66:69], v[142:145], v[216:219], v[66:69]
	s_branch .Lcj1_287
.Lcz2_287:
	v_mfma_f32_16x16x32_bf16 v[62:65], v[146:149], v[174:177], 0
	v_mfma_f32_16x16x32_bf16 v[58:61], v[154:157], v[174:177], 0
	v_mfma_f32_16x16x32_bf16 v[46:49], v[146:149], v[182:185], 0
	v_mfma_f32_16x16x32_bf16 v[42:45], v[154:157], v[182:185], 0
	v_mfma_f32_16x16x32_bf16 v[30:33], v[146:149], v[190:193], 0
	v_mfma_f32_16x16x32_bf16 v[26:29], v[154:157], v[190:193], 0
	v_mfma_f32_16x16x32_bf16 v[14:17], v[146:149], v[200:203], 0
	v_mfma_f32_16x16x32_bf16 v[10:13], v[154:157], v[200:203], 0
	v_mfma_f32_16x16x32_bf16 v[62:65], v[150:153], v[178:181], v[62:65]
	v_mfma_f32_16x16x32_bf16 v[58:61], v[158:161], v[178:181], v[58:61]
	v_mfma_f32_16x16x32_bf16 v[46:49], v[150:153], v[186:189], v[46:49]
	v_mfma_f32_16x16x32_bf16 v[42:45], v[158:161], v[186:189], v[42:45]
	v_mfma_f32_16x16x32_bf16 v[30:33], v[150:153], v[196:199], v[30:33]
	v_mfma_f32_16x16x32_bf16 v[26:29], v[158:161], v[196:199], v[26:29]
	v_mfma_f32_16x16x32_bf16 v[14:17], v[150:153], v[216:219], v[14:17]
	v_mfma_f32_16x16x32_bf16 v[10:13], v[158:161], v[216:219], v[10:13]
	v_mfma_f32_16x16x32_bf16 v[54:57], v[130:133], v[174:177], 0
	v_mfma_f32_16x16x32_bf16 v[50:53], v[138:141], v[174:177], 0
	v_mfma_f32_16x16x32_bf16 v[38:41], v[130:133], v[182:185], 0
	v_mfma_f32_16x16x32_bf16 v[34:37], v[138:141], v[182:185], 0
	v_mfma_f32_16x16x32_bf16 v[22:25], v[130:133], v[190:193], 0
	v_mfma_f32_16x16x32_bf16 v[18:21], v[138:141], v[190:193], 0
	v_mfma_f32_16x16x32_bf16 v[6:9], v[130:133], v[200:203], 0
	v_mfma_f32_16x16x32_bf16 v[2:5], v[138:141], v[200:203], 0
	v_mfma_f32_16x16x32_bf16 v[54:57], v[134:137], v[178:181], v[54:57]
	v_mfma_f32_16x16x32_bf16 v[50:53], v[142:145], v[178:181], v[50:53]
	v_mfma_f32_16x16x32_bf16 v[38:41], v[134:137], v[186:189], v[38:41]
	v_mfma_f32_16x16x32_bf16 v[34:37], v[142:145], v[186:189], v[34:37]
	v_mfma_f32_16x16x32_bf16 v[22:25], v[134:137], v[196:199], v[22:25]
	v_mfma_f32_16x16x32_bf16 v[18:21], v[142:145], v[196:199], v[18:21]
	v_mfma_f32_16x16x32_bf16 v[6:9], v[134:137], v[216:219], v[6:9]
	v_mfma_f32_16x16x32_bf16 v[2:5], v[142:145], v[216:219], v[2:5]
	s_mov_b32 s100, 0
	s_branch .Lcj2_287

.LBB0_374:
	v_add_u32_e32 v142, 0x10000, v217
	v_add_u32_e32 v158, 0x14000, v217
	ds_read_b128 v[130:133], v142
	ds_read_b128 v[134:137], v142 offset:1024
	ds_read_b128 v[138:141], v142 offset:2048
	ds_read_b128 v[142:145], v142 offset:3072
	ds_read_b128 v[146:149], v158
	ds_read_b128 v[150:153], v158 offset:1024
	ds_read_b128 v[154:157], v158 offset:2048
	ds_read_b128 v[158:161], v158 offset:3072
	s_add_i32 m0, s37, 0xc000
	s_add_i32 s57, s37, 0xe000
	s_cmp_eq_u32 s54, s56
	s_cselect_b64 s[58:59], -1, 0
	v_lshl_add_u64 v[196:197], s[20:21], 0, v[194:195]
	v_lshl_add_u64 v[196:197], v[196:197], 0, s[24:25]
	v_mov_b32_e32 v219, v195
	ds_read_b128 v[162:165], v221
	ds_read_b128 v[166:169], v221 offset:1024
	ds_read_b128 v[170:173], v221 offset:2048
	ds_read_b128 v[174:177], v221 offset:3072
	ds_read_b128 v[178:181], v221 offset:4096
	ds_read_b128 v[182:185], v221 offset:5120
	ds_read_b128 v[186:189], v221 offset:6144
	ds_read_b128 v[190:193], v221 offset:7168
	global_load_lds_dwordx4 v[196:197], off
	v_lshl_add_u64 v[196:197], s[20:21], 0, v[218:219]
	v_lshl_add_u64 v[196:197], v[196:197], 0, s[24:25]
	s_mov_b32 m0, s57
	s_nop 0
	global_load_lds_dwordx4 v[196:197], off
	s_cmp_lg_u32 s100, 0
	s_waitcnt vmcnt(8)
	s_waitcnt lgkmcnt(0)
	s_barrier
	s_setprio 1
	s_waitcnt lgkmcnt(0)
	s_cbranch_scc1 .Lcz1_374
	v_mfma_f32_16x16x32_bf16 v[126:129], v[130:133], v[162:165], v[126:129]
	v_mfma_f32_16x16x32_bf16 v[122:125], v[138:141], v[162:165], v[122:125]
	v_mfma_f32_16x16x32_bf16 v[94:97], v[130:133], v[170:173], v[94:97]
	v_mfma_f32_16x16x32_bf16 v[86:89], v[138:141], v[170:173], v[86:89]
	v_mfma_f32_16x16x32_bf16 v[62:65], v[130:133], v[178:181], v[62:65]
	v_mfma_f32_16x16x32_bf16 v[54:57], v[138:141], v[178:181], v[54:57]
	v_mfma_f32_16x16x32_bf16 v[30:33], v[130:133], v[186:189], v[30:33]
	v_mfma_f32_16x16x32_bf16 v[22:25], v[138:141], v[186:189], v[22:25]
	v_mfma_f32_16x16x32_bf16 v[126:129], v[134:137], v[166:169], v[126:129]
	v_mfma_f32_16x16x32_bf16 v[122:125], v[142:145], v[166:169], v[122:125]
	v_mfma_f32_16x16x32_bf16 v[94:97], v[134:137], v[174:177], v[94:97]
	v_mfma_f32_16x16x32_bf16 v[86:89], v[142:145], v[174:177], v[86:89]
	v_mfma_f32_16x16x32_bf16 v[62:65], v[134:137], v[182:185], v[62:65]
	v_mfma_f32_16x16x32_bf16 v[54:57], v[142:145], v[182:185], v[54:57]
	v_mfma_f32_16x16x32_bf16 v[30:33], v[134:137], v[190:193], v[30:33]
	v_mfma_f32_16x16x32_bf16 v[22:25], v[142:145], v[190:193], v[22:25]
	v_mfma_f32_16x16x32_bf16 v[110:113], v[146:149], v[162:165], v[110:113]
	v_mfma_f32_16x16x32_bf16 v[102:105], v[154:157], v[162:165], v[102:105]
	v_mfma_f32_16x16x32_bf16 v[78:81], v[146:149], v[170:173], v[78:81]
	v_mfma_f32_16x16x32_bf16 v[70:73], v[154:157], v[170:173], v[70:73]
	v_mfma_f32_16x16x32_bf16 v[46:49], v[146:149], v[178:181], v[46:49]
	v_mfma_f32_16x16x32_bf16 v[38:41], v[154:157], v[178:181], v[38:41]
	v_mfma_f32_16x16x32_bf16 v[14:17], v[146:149], v[186:189], v[14:17]
	v_mfma_f32_16x16x32_bf16 v[6:9], v[154:157], v[186:189], v[6:9]
	v_mfma_f32_16x16x32_bf16 v[110:113], v[150:153], v[166:169], v[110:113]
	v_mfma_f32_16x16x32_bf16 v[102:105], v[158:161], v[166:169], v[102:105]
	v_mfma_f32_16x16x32_bf16 v[78:81], v[150:153], v[174:177], v[78:81]
	v_mfma_f32_16x16x32_bf16 v[70:73], v[158:161], v[174:177], v[70:73]
	v_mfma_f32_16x16x32_bf16 v[46:49], v[150:153], v[182:185], v[46:49]
	v_mfma_f32_16x16x32_bf16 v[38:41], v[158:161], v[182:185], v[38:41]
	v_mfma_f32_16x16x32_bf16 v[14:17], v[150:153], v[190:193], v[14:17]
	v_mfma_f32_16x16x32_bf16 v[6:9], v[158:161], v[190:193], v[6:9]
.Lcj1_374:
	s_setprio 0
	s_barrier
	s_and_b64 s[60:61], s[58:59], exec
	s_cselect_b32 s62, 0, s56
	s_and_b64 s[58:59], s[2:3], s[58:59]
	s_and_b64 s[58:59], s[58:59], exec
	s_cselect_b32 s9, s55, s9
	s_cselect_b32 s8, s23, s8
	s_cselect_b32 s21, s7, s21
	s_cselect_b32 s20, s6, s20
	s_lshl_b64 s[58:59], s[62:63], 7
	s_add_u32 s60, s8, s58
	s_addc_u32 s61, s9, s59
	s_mov_b32 m0, s38
	s_add_u32 s57, s8, 0x8000
	ds_read_b128 v[162:165], v221 offset:16384
	ds_read_b128 v[166:169], v221 offset:17408
	ds_read_b128 v[170:173], v221 offset:18432
	ds_read_b128 v[174:177], v221 offset:19456
	ds_read_b128 v[178:181], v221 offset:20480
	ds_read_b128 v[182:185], v221 offset:21504
	ds_read_b128 v[186:189], v221 offset:22528
	ds_read_b128 v[190:193], v221 offset:23552
	global_load_lds_dwordx4 v216, s[60:61]
	s_mov_b32 m0, s39
	s_addc_u32 s66, s9, 0
	global_load_lds_dwordx4 v220, s[60:61]
	s_add_u32 s60, s57, s58
	s_addc_u32 s61, s66, s59
	s_mov_b32 m0, s40
	s_add_u32 s58, s20, s58
	global_load_lds_dwordx4 v216, s[60:61]
	s_mov_b32 m0, s41
	s_addc_u32 s59, s21, s59
	global_load_lds_dwordx4 v220, s[60:61]
	s_mov_b32 m0, s37
	s_nop 0
	global_load_lds_dwordx4 v194, s[58:59]
	s_mov_b32 m0, s42
	s_nop 0
	global_load_lds_dwordx4 v218, s[58:59]
	s_cmp_lg_u32 s100, 0
	s_waitcnt vmcnt(8)
	s_waitcnt lgkmcnt(0)
	s_barrier
	s_setprio 1
	s_waitcnt lgkmcnt(0)
	s_cbranch_scc1 .Lcz2_374
	v_mfma_f32_16x16x32_bf16 v[118:121], v[130:133], v[162:165], v[118:121]
	v_mfma_f32_16x16x32_bf16 v[114:117], v[138:141], v[162:165], v[114:117]
	v_mfma_f32_16x16x32_bf16 v[90:93], v[130:133], v[170:173], v[90:93]
	v_mfma_f32_16x16x32_bf16 v[82:85], v[138:141], v[170:173], v[82:85]
	v_mfma_f32_16x16x32_bf16 v[58:61], v[130:133], v[178:181], v[58:61]
	v_mfma_f32_16x16x32_bf16 v[50:53], v[138:141], v[178:181], v[50:53]
	v_mfma_f32_16x16x32_bf16 v[26:29], v[130:133], v[186:189], v[26:29]
	v_mfma_f32_16x16x32_bf16 v[18:21], v[138:141], v[186:189], v[18:21]
	v_mfma_f32_16x16x32_bf16 v[118:121], v[134:137], v[166:169], v[118:121]
	v_mfma_f32_16x16x32_bf16 v[114:117], v[142:145], v[166:169], v[114:117]
	v_mfma_f32_16x16x32_bf16 v[90:93], v[134:137], v[174:177], v[90:93]
	v_mfma_f32_16x16x32_bf16 v[82:85], v[142:145], v[174:177], v[82:85]
	v_mfma_f32_16x16x32_bf16 v[58:61], v[134:137], v[182:185], v[58:61]
	v_mfma_f32_16x16x32_bf16 v[50:53], v[142:145], v[182:185], v[50:53]
	v_mfma_f32_16x16x32_bf16 v[26:29], v[134:137], v[190:193], v[26:29]
	v_mfma_f32_16x16x32_bf16 v[18:21], v[142:145], v[190:193], v[18:21]
	v_mfma_f32_16x16x32_bf16 v[106:109], v[146:149], v[162:165], v[106:109]
	v_mfma_f32_16x16x32_bf16 v[98:101], v[154:157], v[162:165], v[98:101]
	v_mfma_f32_16x16x32_bf16 v[74:77], v[146:149], v[170:173], v[74:77]
	v_mfma_f32_16x16x32_bf16 v[66:69], v[154:157], v[170:173], v[66:69]
	v_mfma_f32_16x16x32_bf16 v[42:45], v[146:149], v[178:181], v[42:45]
	v_mfma_f32_16x16x32_bf16 v[34:37], v[154:157], v[178:181], v[34:37]
	v_mfma_f32_16x16x32_bf16 v[10:13], v[146:149], v[186:189], v[10:13]
	v_mfma_f32_16x16x32_bf16 v[2:5], v[154:157], v[186:189], v[2:5]
	v_mfma_f32_16x16x32_bf16 v[106:109], v[150:153], v[166:169], v[106:109]
	v_mfma_f32_16x16x32_bf16 v[98:101], v[158:161], v[166:169], v[98:101]
	v_mfma_f32_16x16x32_bf16 v[74:77], v[150:153], v[174:177], v[74:77]
	v_mfma_f32_16x16x32_bf16 v[66:69], v[158:161], v[174:177], v[66:69]
	v_mfma_f32_16x16x32_bf16 v[42:45], v[150:153], v[182:185], v[42:45]
	v_mfma_f32_16x16x32_bf16 v[34:37], v[158:161], v[182:185], v[34:37]
	v_mfma_f32_16x16x32_bf16 v[10:13], v[150:153], v[190:193], v[10:13]
	v_mfma_f32_16x16x32_bf16 v[2:5], v[158:161], v[190:193], v[2:5]
.Lcj2_374:
	s_setprio 0
	s_barrier
	v_add_u32_e32 v142, 0x18000, v217
	v_add_u32_e32 v158, 0x1c000, v217
	ds_read_b128 v[130:133], v142
	ds_read_b128 v[134:137], v142 offset:1024
	ds_read_b128 v[138:141], v142 offset:2048
	ds_read_b128 v[142:145], v142 offset:3072
	ds_read_b128 v[146:149], v158
	ds_read_b128 v[150:153], v158 offset:1024
	ds_read_b128 v[154:157], v158 offset:2048
	ds_read_b128 v[158:161], v158 offset:3072
	s_add_u32 s58, s58, 0x8000
	s_addc_u32 s59, s59, 0
	s_mov_b32 m0, s43
	ds_read_b128 v[162:165], v221 offset:32768
	ds_read_b128 v[166:169], v221 offset:33792
	ds_read_b128 v[170:173], v221 offset:34816
	ds_read_b128 v[174:177], v221 offset:35840
	ds_read_b128 v[178:181], v221 offset:36864
	ds_read_b128 v[182:185], v221 offset:37888
	ds_read_b128 v[186:189], v221 offset:38912
	ds_read_b128 v[190:193], v221 offset:39936
	global_load_lds_dwordx4 v194, s[58:59]
	s_mov_b32 m0, s44
	s_nop 0
	global_load_lds_dwordx4 v218, s[58:59]
	s_waitcnt vmcnt(8)
	s_waitcnt lgkmcnt(0)
	s_barrier
	s_setprio 1
	s_waitcnt lgkmcnt(0)
	v_mfma_f32_16x16x32_bf16 v[126:129], v[130:133], v[162:165], v[126:129]
	v_mfma_f32_16x16x32_bf16 v[122:125], v[138:141], v[162:165], v[122:125]
	v_mfma_f32_16x16x32_bf16 v[94:97], v[130:133], v[170:173], v[94:97]
	v_mfma_f32_16x16x32_bf16 v[86:89], v[138:141], v[170:173], v[86:89]
	v_mfma_f32_16x16x32_bf16 v[62:65], v[130:133], v[178:181], v[62:65]
	v_mfma_f32_16x16x32_bf16 v[54:57], v[138:141], v[178:181], v[54:57]
	v_mfma_f32_16x16x32_bf16 v[30:33], v[130:133], v[186:189], v[30:33]
	v_mfma_f32_16x16x32_bf16 v[22:25], v[138:141], v[186:189], v[22:25]
	v_mfma_f32_16x16x32_bf16 v[126:129], v[134:137], v[166:169], v[126:129]
	v_mfma_f32_16x16x32_bf16 v[122:125], v[142:145], v[166:169], v[122:125]
	v_mfma_f32_16x16x32_bf16 v[94:97], v[134:137], v[174:177], v[94:97]
	v_mfma_f32_16x16x32_bf16 v[86:89], v[142:145], v[174:177], v[86:89]
	v_mfma_f32_16x16x32_bf16 v[62:65], v[134:137], v[182:185], v[62:65]
	v_mfma_f32_16x16x32_bf16 v[54:57], v[142:145], v[182:185], v[54:57]
	v_mfma_f32_16x16x32_bf16 v[30:33], v[134:137], v[190:193], v[30:33]
	v_mfma_f32_16x16x32_bf16 v[22:25], v[142:145], v[190:193], v[22:25]
	v_mfma_f32_16x16x32_bf16 v[110:113], v[146:149], v[162:165], v[110:113]
	v_mfma_f32_16x16x32_bf16 v[102:105], v[154:157], v[162:165], v[102:105]
	v_mfma_f32_16x16x32_bf16 v[78:81], v[146:149], v[170:173], v[78:81]
	v_mfma_f32_16x16x32_bf16 v[70:73], v[154:157], v[170:173], v[70:73]
	v_mfma_f32_16x16x32_bf16 v[46:49], v[146:149], v[178:181], v[46:49]
	v_mfma_f32_16x16x32_bf16 v[38:41], v[154:157], v[178:181], v[38:41]
	v_mfma_f32_16x16x32_bf16 v[14:17], v[146:149], v[186:189], v[14:17]
	v_mfma_f32_16x16x32_bf16 v[6:9], v[154:157], v[186:189], v[6:9]
	v_mfma_f32_16x16x32_bf16 v[110:113], v[150:153], v[166:169], v[110:113]
	v_mfma_f32_16x16x32_bf16 v[102:105], v[158:161], v[166:169], v[102:105]
	v_mfma_f32_16x16x32_bf16 v[78:81], v[150:153], v[174:177], v[78:81]
	v_mfma_f32_16x16x32_bf16 v[70:73], v[158:161], v[174:177], v[70:73]
	v_mfma_f32_16x16x32_bf16 v[46:49], v[150:153], v[182:185], v[46:49]
	v_mfma_f32_16x16x32_bf16 v[38:41], v[158:161], v[182:185], v[38:41]
	v_mfma_f32_16x16x32_bf16 v[14:17], v[150:153], v[190:193], v[14:17]
	v_mfma_f32_16x16x32_bf16 v[6:9], v[158:161], v[190:193], v[6:9]
	s_setprio 0
	s_barrier
	s_or_b32 s62, s62, 1
	s_lshl_b64 s[58:59], s[62:63], 7
	s_add_u32 s60, s8, s58
	s_mov_b32 m0, s45
	s_addc_u32 s61, s9, s59
	ds_read_b128 v[162:165], v221 offset:49152
	ds_read_b128 v[166:169], v221 offset:50176
	ds_read_b128 v[170:173], v221 offset:51200
	ds_read_b128 v[174:177], v221 offset:52224
	ds_read_b128 v[178:181], v221 offset:53248
	ds_read_b128 v[182:185], v221 offset:54272
	ds_read_b128 v[186:189], v221 offset:55296
	ds_read_b128 v[190:193], v221 offset:56320
	global_load_lds_dwordx4 v216, s[60:61]
	s_mov_b32 m0, s46
	s_nop 0
	global_load_lds_dwordx4 v220, s[60:61]
	s_add_u32 s60, s57, s58
	s_addc_u32 s61, s66, s59
	s_mov_b32 m0, s49
	s_add_u32 s58, s20, s58
	global_load_lds_dwordx4 v216, s[60:61]
	s_mov_b32 m0, s50
	s_addc_u32 s59, s21, s59
	global_load_lds_dwordx4 v220, s[60:61]
	s_mov_b32 m0, s47
	s_nop 0
	global_load_lds_dwordx4 v194, s[58:59]
	s_mov_b32 m0, s48
	s_nop 0
	global_load_lds_dwordx4 v218, s[58:59]
	s_waitcnt vmcnt(8)
	s_waitcnt lgkmcnt(0)
	s_barrier
	s_setprio 1
	s_waitcnt lgkmcnt(0)
	v_mfma_f32_16x16x32_bf16 v[118:121], v[130:133], v[162:165], v[118:121]
	v_mfma_f32_16x16x32_bf16 v[114:117], v[138:141], v[162:165], v[114:117]
	v_mfma_f32_16x16x32_bf16 v[90:93], v[130:133], v[170:173], v[90:93]
	v_mfma_f32_16x16x32_bf16 v[82:85], v[138:141], v[170:173], v[82:85]
	v_mfma_f32_16x16x32_bf16 v[58:61], v[130:133], v[178:181], v[58:61]
	v_mfma_f32_16x16x32_bf16 v[50:53], v[138:141], v[178:181], v[50:53]
	v_mfma_f32_16x16x32_bf16 v[26:29], v[130:133], v[186:189], v[26:29]
	v_mfma_f32_16x16x32_bf16 v[18:21], v[138:141], v[186:189], v[18:21]
	v_mfma_f32_16x16x32_bf16 v[118:121], v[134:137], v[166:169], v[118:121]
	v_mfma_f32_16x16x32_bf16 v[114:117], v[142:145], v[166:169], v[114:117]
	v_mfma_f32_16x16x32_bf16 v[90:93], v[134:137], v[174:177], v[90:93]
	v_mfma_f32_16x16x32_bf16 v[82:85], v[142:145], v[174:177], v[82:85]
	v_mfma_f32_16x16x32_bf16 v[58:61], v[134:137], v[182:185], v[58:61]
	v_mfma_f32_16x16x32_bf16 v[50:53], v[142:145], v[182:185], v[50:53]
	v_mfma_f32_16x16x32_bf16 v[26:29], v[134:137], v[190:193], v[26:29]
	v_mfma_f32_16x16x32_bf16 v[18:21], v[142:145], v[190:193], v[18:21]
	v_mfma_f32_16x16x32_bf16 v[106:109], v[146:149], v[162:165], v[106:109]
	v_mfma_f32_16x16x32_bf16 v[98:101], v[154:157], v[162:165], v[98:101]
	v_mfma_f32_16x16x32_bf16 v[74:77], v[146:149], v[170:173], v[74:77]
	v_mfma_f32_16x16x32_bf16 v[66:69], v[154:157], v[170:173], v[66:69]
	v_mfma_f32_16x16x32_bf16 v[42:45], v[146:149], v[178:181], v[42:45]
	v_mfma_f32_16x16x32_bf16 v[34:37], v[154:157], v[178:181], v[34:37]
	v_mfma_f32_16x16x32_bf16 v[10:13], v[146:149], v[186:189], v[10:13]
	v_mfma_f32_16x16x32_bf16 v[2:5], v[154:157], v[186:189], v[2:5]
	v_mfma_f32_16x16x32_bf16 v[106:109], v[150:153], v[166:169], v[106:109]
	v_mfma_f32_16x16x32_bf16 v[98:101], v[158:161], v[166:169], v[98:101]
	v_mfma_f32_16x16x32_bf16 v[74:77], v[150:153], v[174:177], v[74:77]
	v_mfma_f32_16x16x32_bf16 v[66:69], v[158:161], v[174:177], v[66:69]
	v_mfma_f32_16x16x32_bf16 v[42:45], v[150:153], v[182:185], v[42:45]
	v_mfma_f32_16x16x32_bf16 v[34:37], v[158:161], v[182:185], v[34:37]
	v_mfma_f32_16x16x32_bf16 v[10:13], v[150:153], v[190:193], v[10:13]
	v_mfma_f32_16x16x32_bf16 v[2:5], v[158:161], v[190:193], v[2:5]
	s_setprio 0
	s_barrier
	s_add_i32 s57, s56, 2
	s_add_u32 s24, s24, 0x100
	s_addc_u32 s25, s25, 0
	s_cmp_ge_i32 s56, s54
	s_mov_b32 s56, s57
	s_cbranch_scc0 .LBB0_374
	s_branch .Lcsk_374
.Lcz1_374:
	v_mfma_f32_16x16x32_bf16 v[126:129], v[130:133], v[162:165], 0
	v_mfma_f32_16x16x32_bf16 v[122:125], v[138:141], v[162:165], 0
	v_mfma_f32_16x16x32_bf16 v[94:97], v[130:133], v[170:173], 0
	v_mfma_f32_16x16x32_bf16 v[86:89], v[138:141], v[170:173], 0
	v_mfma_f32_16x16x32_bf16 v[62:65], v[130:133], v[178:181], 0
	v_mfma_f32_16x16x32_bf16 v[54:57], v[138:141], v[178:181], 0
	v_mfma_f32_16x16x32_bf16 v[30:33], v[130:133], v[186:189], 0
	v_mfma_f32_16x16x32_bf16 v[22:25], v[138:141], v[186:189], 0
	v_mfma_f32_16x16x32_bf16 v[126:129], v[134:137], v[166:169], v[126:129]
	v_mfma_f32_16x16x32_bf16 v[122:125], v[142:145], v[166:169], v[122:125]
	v_mfma_f32_16x16x32_bf16 v[94:97], v[134:137], v[174:177], v[94:97]
	v_mfma_f32_16x16x32_bf16 v[86:89], v[142:145], v[174:177], v[86:89]
	v_mfma_f32_16x16x32_bf16 v[62:65], v[134:137], v[182:185], v[62:65]
	v_mfma_f32_16x16x32_bf16 v[54:57], v[142:145], v[182:185], v[54:57]
	v_mfma_f32_16x16x32_bf16 v[30:33], v[134:137], v[190:193], v[30:33]
	v_mfma_f32_16x16x32_bf16 v[22:25], v[142:145], v[190:193], v[22:25]
	v_mfma_f32_16x16x32_bf16 v[110:113], v[146:149], v[162:165], 0
	v_mfma_f32_16x16x32_bf16 v[102:105], v[154:157], v[162:165], 0
	v_mfma_f32_16x16x32_bf16 v[78:81], v[146:149], v[170:173], 0
	v_mfma_f32_16x16x32_bf16 v[70:73], v[154:157], v[170:173], 0
	v_mfma_f32_16x16x32_bf16 v[46:49], v[146:149], v[178:181], 0
	v_mfma_f32_16x16x32_bf16 v[38:41], v[154:157], v[178:181], 0
	v_mfma_f32_16x16x32_bf16 v[14:17], v[146:149], v[186:189], 0
	v_mfma_f32_16x16x32_bf16 v[6:9], v[154:157], v[186:189], 0
	v_mfma_f32_16x16x32_bf16 v[110:113], v[150:153], v[166:169], v[110:113]
	v_mfma_f32_16x16x32_bf16 v[102:105], v[158:161], v[166:169], v[102:105]
	v_mfma_f32_16x16x32_bf16 v[78:81], v[150:153], v[174:177], v[78:81]
	v_mfma_f32_16x16x32_bf16 v[70:73], v[158:161], v[174:177], v[70:73]
	v_mfma_f32_16x16x32_bf16 v[46:49], v[150:153], v[182:185], v[46:49]
	v_mfma_f32_16x16x32_bf16 v[38:41], v[158:161], v[182:185], v[38:41]
	v_mfma_f32_16x16x32_bf16 v[14:17], v[150:153], v[190:193], v[14:17]
	v_mfma_f32_16x16x32_bf16 v[6:9], v[158:161], v[190:193], v[6:9]
	s_branch .Lcj1_374
.Lcz2_374:
	v_mfma_f32_16x16x32_bf16 v[118:121], v[130:133], v[162:165], 0
	v_mfma_f32_16x16x32_bf16 v[114:117], v[138:141], v[162:165], 0
	v_mfma_f32_16x16x32_bf16 v[90:93], v[130:133], v[170:173], 0
	v_mfma_f32_16x16x32_bf16 v[82:85], v[138:141], v[170:173], 0
	v_mfma_f32_16x16x32_bf16 v[58:61], v[130:133], v[178:181], 0
	v_mfma_f32_16x16x32_bf16 v[50:53], v[138:141], v[178:181], 0
	v_mfma_f32_16x16x32_bf16 v[26:29], v[130:133], v[186:189], 0
	v_mfma_f32_16x16x32_bf16 v[18:21], v[138:141], v[186:189], 0
	v_mfma_f32_16x16x32_bf16 v[118:121], v[134:137], v[166:169], v[118:121]
	v_mfma_f32_16x16x32_bf16 v[114:117], v[142:145], v[166:169], v[114:117]
	v_mfma_f32_16x16x32_bf16 v[90:93], v[134:137], v[174:177], v[90:93]
	v_mfma_f32_16x16x32_bf16 v[82:85], v[142:145], v[174:177], v[82:85]
	v_mfma_f32_16x16x32_bf16 v[58:61], v[134:137], v[182:185], v[58:61]
	v_mfma_f32_16x16x32_bf16 v[50:53], v[142:145], v[182:185], v[50:53]
	v_mfma_f32_16x16x32_bf16 v[26:29], v[134:137], v[190:193], v[26:29]
	v_mfma_f32_16x16x32_bf16 v[18:21], v[142:145], v[190:193], v[18:21]
	v_mfma_f32_16x16x32_bf16 v[106:109], v[146:149], v[162:165], 0
	v_mfma_f32_16x16x32_bf16 v[98:101], v[154:157], v[162:165], 0
	v_mfma_f32_16x16x32_bf16 v[74:77], v[146:149], v[170:173], 0
	v_mfma_f32_16x16x32_bf16 v[66:69], v[154:157], v[170:173], 0
	v_mfma_f32_16x16x32_bf16 v[42:45], v[146:149], v[178:181], 0
	v_mfma_f32_16x16x32_bf16 v[34:37], v[154:157], v[178:181], 0
	v_mfma_f32_16x16x32_bf16 v[10:13], v[146:149], v[186:189], 0
	v_mfma_f32_16x16x32_bf16 v[2:5], v[154:157], v[186:189], 0
	v_mfma_f32_16x16x32_bf16 v[106:109], v[150:153], v[166:169], v[106:109]
	v_mfma_f32_16x16x32_bf16 v[98:101], v[158:161], v[166:169], v[98:101]
	v_mfma_f32_16x16x32_bf16 v[74:77], v[150:153], v[174:177], v[74:77]
	v_mfma_f32_16x16x32_bf16 v[66:69], v[158:161], v[174:177], v[66:69]
	v_mfma_f32_16x16x32_bf16 v[42:45], v[150:153], v[182:185], v[42:45]
	v_mfma_f32_16x16x32_bf16 v[34:37], v[158:161], v[182:185], v[34:37]
	v_mfma_f32_16x16x32_bf16 v[10:13], v[150:153], v[190:193], v[10:13]
	v_mfma_f32_16x16x32_bf16 v[2:5], v[158:161], v[190:193], v[2:5]
	s_mov_b32 s100, 0
	s_branch .Lcj2_374

.LBB0_492:
	v_add_u32_e32 v130, 0x10000, v165
	v_add_u32_e32 v142, 0x14000, v165
	ds_read_b128 v[146:149], v130
	ds_read_b128 v[150:153], v130 offset:1024
	ds_read_b128 v[154:157], v130 offset:2048
	ds_read_b128 v[158:161], v130 offset:3072
	ds_read_b128 v[130:133], v142
	ds_read_b128 v[134:137], v142 offset:1024
	ds_read_b128 v[138:141], v142 offset:2048
	ds_read_b128 v[142:145], v142 offset:3072
	s_add_i32 m0, s29, 0xc000
	s_add_i32 s24, s29, 0xe000
	s_cmp_lg_u32 s52, s55
	s_cselect_b64 s[56:57], -1, 0
	v_lshl_add_u64 v[204:205], s[16:17], 0, v[194:195]
	v_lshl_add_u64 v[204:205], v[204:205], 0, s[22:23]
	v_mov_b32_e32 v163, v195
	ds_read_b128 v[174:177], v167
	ds_read_b128 v[178:181], v167 offset:1024
	ds_read_b128 v[182:185], v167 offset:2048
	ds_read_b128 v[186:189], v167 offset:3072
	ds_read_b128 v[190:193], v167 offset:4096
	ds_read_b128 v[196:199], v167 offset:5120
	ds_read_b128 v[200:203], v167 offset:6144
	ds_read_b128 v[216:219], v167 offset:7168
	global_load_lds_dwordx4 v[204:205], off
	v_lshl_add_u64 v[204:205], s[16:17], 0, v[162:163]
	v_lshl_add_u64 v[204:205], v[204:205], 0, s[22:23]
	s_mov_b32 m0, s24
	s_nop 0
	global_load_lds_dwordx4 v[204:205], off
	s_cmp_lg_u32 s100, 0
	s_waitcnt vmcnt(8)
	s_waitcnt lgkmcnt(0)
	s_barrier
	s_setprio 1
	s_waitcnt lgkmcnt(0)
	s_cbranch_scc1 .Lcz1_492
	v_mfma_f32_16x16x32_bf16 v[126:129], v[146:149], v[174:177], v[126:129]
	v_mfma_f32_16x16x32_bf16 v[122:125], v[154:157], v[174:177], v[122:125]
	v_mfma_f32_16x16x32_bf16 v[110:113], v[146:149], v[182:185], v[110:113]
	v_mfma_f32_16x16x32_bf16 v[106:109], v[154:157], v[182:185], v[106:109]
	v_mfma_f32_16x16x32_bf16 v[94:97], v[146:149], v[190:193], v[94:97]
	v_mfma_f32_16x16x32_bf16 v[90:93], v[154:157], v[190:193], v[90:93]
	v_mfma_f32_16x16x32_bf16 v[78:81], v[146:149], v[200:203], v[78:81]
	v_mfma_f32_16x16x32_bf16 v[74:77], v[154:157], v[200:203], v[74:77]
	v_mfma_f32_16x16x32_bf16 v[126:129], v[150:153], v[178:181], v[126:129]
	v_mfma_f32_16x16x32_bf16 v[122:125], v[158:161], v[178:181], v[122:125]
	v_mfma_f32_16x16x32_bf16 v[110:113], v[150:153], v[186:189], v[110:113]
	v_mfma_f32_16x16x32_bf16 v[106:109], v[158:161], v[186:189], v[106:109]
	v_mfma_f32_16x16x32_bf16 v[94:97], v[150:153], v[196:199], v[94:97]
	v_mfma_f32_16x16x32_bf16 v[90:93], v[158:161], v[196:199], v[90:93]
	v_mfma_f32_16x16x32_bf16 v[78:81], v[150:153], v[216:219], v[78:81]
	v_mfma_f32_16x16x32_bf16 v[74:77], v[158:161], v[216:219], v[74:77]
	v_mfma_f32_16x16x32_bf16 v[118:121], v[130:133], v[174:177], v[118:121]
	v_mfma_f32_16x16x32_bf16 v[114:117], v[138:141], v[174:177], v[114:117]
	v_mfma_f32_16x16x32_bf16 v[102:105], v[130:133], v[182:185], v[102:105]
	v_mfma_f32_16x16x32_bf16 v[98:101], v[138:141], v[182:185], v[98:101]
	v_mfma_f32_16x16x32_bf16 v[86:89], v[130:133], v[190:193], v[86:89]
	v_mfma_f32_16x16x32_bf16 v[82:85], v[138:141], v[190:193], v[82:85]
	v_mfma_f32_16x16x32_bf16 v[70:73], v[130:133], v[200:203], v[70:73]
	v_mfma_f32_16x16x32_bf16 v[66:69], v[138:141], v[200:203], v[66:69]
	v_mfma_f32_16x16x32_bf16 v[118:121], v[134:137], v[178:181], v[118:121]
	v_mfma_f32_16x16x32_bf16 v[114:117], v[142:145], v[178:181], v[114:117]
	v_mfma_f32_16x16x32_bf16 v[102:105], v[134:137], v[186:189], v[102:105]
	v_mfma_f32_16x16x32_bf16 v[98:101], v[142:145], v[186:189], v[98:101]
	v_mfma_f32_16x16x32_bf16 v[86:89], v[134:137], v[196:199], v[86:89]
	v_mfma_f32_16x16x32_bf16 v[82:85], v[142:145], v[196:199], v[82:85]
	v_mfma_f32_16x16x32_bf16 v[70:73], v[134:137], v[216:219], v[70:73]
	v_mfma_f32_16x16x32_bf16 v[66:69], v[142:145], v[216:219], v[66:69]

.LBB0_494:
	s_ashr_i32 s25, s24, 31
	s_lshl_b64 s[24:25], s[24:25], 7
	s_add_u32 s56, s14, s24
	s_mov_b32 m0, s30
	s_addc_u32 s57, s15, s25
	ds_read_b128 v[174:177], v167 offset:16384
	ds_read_b128 v[178:181], v167 offset:17408
	ds_read_b128 v[182:185], v167 offset:18432
	ds_read_b128 v[186:189], v167 offset:19456
	ds_read_b128 v[190:193], v167 offset:20480
	ds_read_b128 v[196:199], v167 offset:21504
	ds_read_b128 v[200:203], v167 offset:22528
	ds_read_b128 v[216:219], v167 offset:23552
	global_load_lds_dwordx4 v164, s[56:57]
	s_mov_b32 m0, s31
	s_nop 0
	global_load_lds_dwordx4 v168, s[56:57]
	s_mov_b32 m0, s37
	s_nop 0
	global_load_lds_dwordx4 v166, s[56:57]
	s_mov_b32 m0, s38
	s_nop 0
	global_load_lds_dwordx4 v170, s[56:57]
	s_add_u32 s56, s16, s24
	s_addc_u32 s57, s17, s25
	v_lshl_add_u64 v[204:205], s[56:57], 0, v[194:195]
	s_mov_b32 m0, s29
	s_nop 0
	global_load_lds_dwordx4 v[204:205], off
	v_lshl_add_u64 v[204:205], s[56:57], 0, v[162:163]
	s_mov_b32 m0, s39
	s_nop 0
	global_load_lds_dwordx4 v[204:205], off
	s_cmp_lg_u32 s100, 0
	s_waitcnt vmcnt(8)
	s_waitcnt lgkmcnt(0)
	s_barrier
	s_setprio 1
	s_waitcnt lgkmcnt(0)
	s_cbranch_scc1 .Lcz2_492
	v_mfma_f32_16x16x32_bf16 v[62:65], v[146:149], v[174:177], v[62:65]
	v_mfma_f32_16x16x32_bf16 v[58:61], v[154:157], v[174:177], v[58:61]
	v_mfma_f32_16x16x32_bf16 v[46:49], v[146:149], v[182:185], v[46:49]
	v_mfma_f32_16x16x32_bf16 v[42:45], v[154:157], v[182:185], v[42:45]
	v_mfma_f32_16x16x32_bf16 v[30:33], v[146:149], v[190:193], v[30:33]
	v_mfma_f32_16x16x32_bf16 v[26:29], v[154:157], v[190:193], v[26:29]
	v_mfma_f32_16x16x32_bf16 v[14:17], v[146:149], v[200:203], v[14:17]
	v_mfma_f32_16x16x32_bf16 v[10:13], v[154:157], v[200:203], v[10:13]
	v_mfma_f32_16x16x32_bf16 v[62:65], v[150:153], v[178:181], v[62:65]
	v_mfma_f32_16x16x32_bf16 v[58:61], v[158:161], v[178:181], v[58:61]
	v_mfma_f32_16x16x32_bf16 v[46:49], v[150:153], v[186:189], v[46:49]
	v_mfma_f32_16x16x32_bf16 v[42:45], v[158:161], v[186:189], v[42:45]
	v_mfma_f32_16x16x32_bf16 v[30:33], v[150:153], v[196:199], v[30:33]
	v_mfma_f32_16x16x32_bf16 v[26:29], v[158:161], v[196:199], v[26:29]
	v_mfma_f32_16x16x32_bf16 v[14:17], v[150:153], v[216:219], v[14:17]
	v_mfma_f32_16x16x32_bf16 v[10:13], v[158:161], v[216:219], v[10:13]
	v_mfma_f32_16x16x32_bf16 v[54:57], v[130:133], v[174:177], v[54:57]
	v_mfma_f32_16x16x32_bf16 v[50:53], v[138:141], v[174:177], v[50:53]
	v_mfma_f32_16x16x32_bf16 v[38:41], v[130:133], v[182:185], v[38:41]
	v_mfma_f32_16x16x32_bf16 v[34:37], v[138:141], v[182:185], v[34:37]
	v_mfma_f32_16x16x32_bf16 v[22:25], v[130:133], v[190:193], v[22:25]
	v_mfma_f32_16x16x32_bf16 v[18:21], v[138:141], v[190:193], v[18:21]
	v_mfma_f32_16x16x32_bf16 v[6:9], v[130:133], v[200:203], v[6:9]
	v_mfma_f32_16x16x32_bf16 v[2:5], v[138:141], v[200:203], v[2:5]
	v_mfma_f32_16x16x32_bf16 v[54:57], v[134:137], v[178:181], v[54:57]
	v_mfma_f32_16x16x32_bf16 v[50:53], v[142:145], v[178:181], v[50:53]
	v_mfma_f32_16x16x32_bf16 v[38:41], v[134:137], v[186:189], v[38:41]
	v_mfma_f32_16x16x32_bf16 v[34:37], v[142:145], v[186:189], v[34:37]
	v_mfma_f32_16x16x32_bf16 v[22:25], v[134:137], v[196:199], v[22:25]
	v_mfma_f32_16x16x32_bf16 v[18:21], v[142:145], v[196:199], v[18:21]
	v_mfma_f32_16x16x32_bf16 v[6:9], v[134:137], v[216:219], v[6:9]
	v_mfma_f32_16x16x32_bf16 v[2:5], v[142:145], v[216:219], v[2:5]
.Lcj2_492:
	s_setprio 0
	s_barrier
	v_add_u32_e32 v142, 0x18000, v165
	v_add_u32_e32 v158, 0x1c000, v165
	ds_read_b128 v[130:133], v142
	ds_read_b128 v[134:137], v142 offset:1024
	ds_read_b128 v[138:141], v142 offset:2048
	ds_read_b128 v[142:145], v142 offset:3072
	ds_read_b128 v[146:149], v158
	ds_read_b128 v[150:153], v158 offset:1024
	ds_read_b128 v[154:157], v158 offset:2048
	ds_read_b128 v[158:161], v158 offset:3072
	s_add_u32 s56, s56, 0x10000
	s_addc_u32 s57, s57, 0
	s_mov_b32 m0, s40
	v_lshl_add_u64 v[204:205], s[56:57], 0, v[194:195]
	ds_read_b128 v[174:177], v167 offset:32768
	ds_read_b128 v[178:181], v167 offset:33792
	ds_read_b128 v[182:185], v167 offset:34816
	ds_read_b128 v[186:189], v167 offset:35840
	ds_read_b128 v[190:193], v167 offset:36864
	ds_read_b128 v[196:199], v167 offset:37888
	ds_read_b128 v[200:203], v167 offset:38912
	ds_read_b128 v[216:219], v167 offset:39936
	global_load_lds_dwordx4 v[204:205], off
	v_lshl_add_u64 v[204:205], s[56:57], 0, v[162:163]
	s_mov_b32 m0, s41
	s_nop 0
	global_load_lds_dwordx4 v[204:205], off
	s_waitcnt vmcnt(8)
	s_waitcnt lgkmcnt(0)
	s_barrier
	s_setprio 1
	s_waitcnt lgkmcnt(0)
	v_mfma_f32_16x16x32_bf16 v[126:129], v[130:133], v[174:177], v[126:129]
	v_mfma_f32_16x16x32_bf16 v[122:125], v[138:141], v[174:177], v[122:125]
	v_mfma_f32_16x16x32_bf16 v[110:113], v[130:133], v[182:185], v[110:113]
	v_mfma_f32_16x16x32_bf16 v[106:109], v[138:141], v[182:185], v[106:109]
	v_mfma_f32_16x16x32_bf16 v[94:97], v[130:133], v[190:193], v[94:97]
	v_mfma_f32_16x16x32_bf16 v[90:93], v[138:141], v[190:193], v[90:93]
	v_mfma_f32_16x16x32_bf16 v[78:81], v[130:133], v[200:203], v[78:81]
	v_mfma_f32_16x16x32_bf16 v[74:77], v[138:141], v[200:203], v[74:77]
	v_mfma_f32_16x16x32_bf16 v[126:129], v[134:137], v[178:181], v[126:129]
	v_mfma_f32_16x16x32_bf16 v[122:125], v[142:145], v[178:181], v[122:125]
	v_mfma_f32_16x16x32_bf16 v[110:113], v[134:137], v[186:189], v[110:113]
	v_mfma_f32_16x16x32_bf16 v[106:109], v[142:145], v[186:189], v[106:109]
	v_mfma_f32_16x16x32_bf16 v[94:97], v[134:137], v[196:199], v[94:97]
	v_mfma_f32_16x16x32_bf16 v[90:93], v[142:145], v[196:199], v[90:93]
	v_mfma_f32_16x16x32_bf16 v[78:81], v[134:137], v[216:219], v[78:81]
	v_mfma_f32_16x16x32_bf16 v[74:77], v[142:145], v[216:219], v[74:77]
	v_mfma_f32_16x16x32_bf16 v[118:121], v[146:149], v[174:177], v[118:121]
	v_mfma_f32_16x16x32_bf16 v[114:117], v[154:157], v[174:177], v[114:117]
	v_mfma_f32_16x16x32_bf16 v[102:105], v[146:149], v[182:185], v[102:105]
	v_mfma_f32_16x16x32_bf16 v[98:101], v[154:157], v[182:185], v[98:101]
	v_mfma_f32_16x16x32_bf16 v[86:89], v[146:149], v[190:193], v[86:89]
	v_mfma_f32_16x16x32_bf16 v[82:85], v[154:157], v[190:193], v[82:85]
	v_mfma_f32_16x16x32_bf16 v[70:73], v[146:149], v[200:203], v[70:73]
	v_mfma_f32_16x16x32_bf16 v[66:69], v[154:157], v[200:203], v[66:69]
	v_mfma_f32_16x16x32_bf16 v[118:121], v[150:153], v[178:181], v[118:121]
	v_mfma_f32_16x16x32_bf16 v[114:117], v[158:161], v[178:181], v[114:117]
	v_mfma_f32_16x16x32_bf16 v[102:105], v[150:153], v[186:189], v[102:105]
	v_mfma_f32_16x16x32_bf16 v[98:101], v[158:161], v[186:189], v[98:101]
	v_mfma_f32_16x16x32_bf16 v[86:89], v[150:153], v[196:199], v[86:89]
	v_mfma_f32_16x16x32_bf16 v[82:85], v[158:161], v[196:199], v[82:85]
	v_mfma_f32_16x16x32_bf16 v[70:73], v[150:153], v[216:219], v[70:73]
	v_mfma_f32_16x16x32_bf16 v[66:69], v[158:161], v[216:219], v[66:69]
	s_setprio 0
	s_barrier
	s_add_u32 s56, s24, 0x80
	s_addc_u32 s57, s25, 0
	s_add_u32 s24, s14, s56
	s_mov_b32 m0, s43
	s_addc_u32 s25, s15, s57
	ds_read_b128 v[174:177], v167 offset:49152
	ds_read_b128 v[178:181], v167 offset:50176
	ds_read_b128 v[182:185], v167 offset:51200
	ds_read_b128 v[186:189], v167 offset:52224
	ds_read_b128 v[190:193], v167 offset:53248
	ds_read_b128 v[196:199], v167 offset:54272
	ds_read_b128 v[200:203], v167 offset:55296
	ds_read_b128 v[216:219], v167 offset:56320
	global_load_lds_dwordx4 v164, s[24:25]
	s_mov_b32 m0, s44
	s_nop 0
	global_load_lds_dwordx4 v168, s[24:25]
	s_mov_b32 m0, s47
	s_nop 0
	global_load_lds_dwordx4 v166, s[24:25]
	s_mov_b32 m0, s48
	s_nop 0
	global_load_lds_dwordx4 v170, s[24:25]
	s_add_u32 s24, s16, s56
	s_addc_u32 s25, s17, s57
	v_lshl_add_u64 v[204:205], s[24:25], 0, v[194:195]
	s_mov_b32 m0, s45
	s_nop 0
	global_load_lds_dwordx4 v[204:205], off
	v_lshl_add_u64 v[204:205], s[24:25], 0, v[162:163]
	s_mov_b32 m0, s46
	s_nop 0
	global_load_lds_dwordx4 v[204:205], off
	s_waitcnt vmcnt(8)
	s_waitcnt lgkmcnt(0)
	s_barrier
	s_setprio 1
	s_waitcnt lgkmcnt(0)
	v_mfma_f32_16x16x32_bf16 v[62:65], v[130:133], v[174:177], v[62:65]
	v_mfma_f32_16x16x32_bf16 v[58:61], v[138:141], v[174:177], v[58:61]
	v_mfma_f32_16x16x32_bf16 v[46:49], v[130:133], v[182:185], v[46:49]
	v_mfma_f32_16x16x32_bf16 v[42:45], v[138:141], v[182:185], v[42:45]
	v_mfma_f32_16x16x32_bf16 v[30:33], v[130:133], v[190:193], v[30:33]
	v_mfma_f32_16x16x32_bf16 v[26:29], v[138:141], v[190:193], v[26:29]
	v_mfma_f32_16x16x32_bf16 v[14:17], v[130:133], v[200:203], v[14:17]
	v_mfma_f32_16x16x32_bf16 v[10:13], v[138:141], v[200:203], v[10:13]
	v_mfma_f32_16x16x32_bf16 v[62:65], v[134:137], v[178:181], v[62:65]
	v_mfma_f32_16x16x32_bf16 v[58:61], v[142:145], v[178:181], v[58:61]
	v_mfma_f32_16x16x32_bf16 v[46:49], v[134:137], v[186:189], v[46:49]
	v_mfma_f32_16x16x32_bf16 v[42:45], v[142:145], v[186:189], v[42:45]
	v_mfma_f32_16x16x32_bf16 v[30:33], v[134:137], v[196:199], v[30:33]
	v_mfma_f32_16x16x32_bf16 v[26:29], v[142:145], v[196:199], v[26:29]
	v_mfma_f32_16x16x32_bf16 v[14:17], v[134:137], v[216:219], v[14:17]
	v_mfma_f32_16x16x32_bf16 v[10:13], v[142:145], v[216:219], v[10:13]
	v_mfma_f32_16x16x32_bf16 v[54:57], v[146:149], v[174:177], v[54:57]
	v_mfma_f32_16x16x32_bf16 v[50:53], v[154:157], v[174:177], v[50:53]
	v_mfma_f32_16x16x32_bf16 v[38:41], v[146:149], v[182:185], v[38:41]
	v_mfma_f32_16x16x32_bf16 v[34:37], v[154:157], v[182:185], v[34:37]
	v_mfma_f32_16x16x32_bf16 v[22:25], v[146:149], v[190:193], v[22:25]
	v_mfma_f32_16x16x32_bf16 v[18:21], v[154:157], v[190:193], v[18:21]
	v_mfma_f32_16x16x32_bf16 v[6:9], v[146:149], v[200:203], v[6:9]
	v_mfma_f32_16x16x32_bf16 v[2:5], v[154:157], v[200:203], v[2:5]
	v_mfma_f32_16x16x32_bf16 v[54:57], v[150:153], v[178:181], v[54:57]
	v_mfma_f32_16x16x32_bf16 v[50:53], v[158:161], v[178:181], v[50:53]
	v_mfma_f32_16x16x32_bf16 v[38:41], v[150:153], v[186:189], v[38:41]
	v_mfma_f32_16x16x32_bf16 v[34:37], v[158:161], v[186:189], v[34:37]
	v_mfma_f32_16x16x32_bf16 v[22:25], v[150:153], v[196:199], v[22:25]
	v_mfma_f32_16x16x32_bf16 v[18:21], v[158:161], v[196:199], v[18:21]
	v_mfma_f32_16x16x32_bf16 v[6:9], v[150:153], v[216:219], v[6:9]
	v_mfma_f32_16x16x32_bf16 v[2:5], v[158:161], v[216:219], v[2:5]
	s_setprio 0
	s_barrier
	s_add_i32 s24, s55, 2
	s_add_u32 s22, s22, 0x100
	s_addc_u32 s23, s23, 0
	s_cmp_ge_i32 s55, s52
	s_cbranch_scc1 .LBB0_497
	s_mov_b32 s55, s24
	s_branch .LBB0_492

.LBB0_581:
	v_add_u32_e32 v142, 0x10000, v191
	v_add_u32_e32 v158, 0x14000, v191
	ds_read_b128 v[130:133], v142
	ds_read_b128 v[134:137], v142 offset:1024
	ds_read_b128 v[138:141], v142 offset:2048
	ds_read_b128 v[142:145], v142 offset:3072
	ds_read_b128 v[146:149], v158
	ds_read_b128 v[150:153], v158 offset:1024
	ds_read_b128 v[154:157], v158 offset:2048
	ds_read_b128 v[158:161], v158 offset:3072
	s_add_i32 m0, s31, 0xc000
	s_add_i32 s62, s31, 0xe000
	s_add_i32 s66, s61, 2
	s_cmp_eq_u32 s59, s61
	s_cselect_b64 s[68:69], -1, 0
	v_lshl_add_u64 v[200:201], s[0:1], 0, v[194:195]
	v_lshl_add_u64 v[200:201], v[200:201], 0, s[22:23]
	v_mov_b32_e32 v193, v195
	ds_read_b128 v[162:165], v217
	ds_read_b128 v[166:169], v217 offset:1024
	ds_read_b128 v[170:173], v217 offset:2048
	ds_read_b128 v[174:177], v217 offset:3072
	ds_read_b128 v[178:181], v217 offset:4096
	ds_read_b128 v[182:185], v217 offset:5120
	ds_read_b128 v[186:189], v217 offset:6144
	ds_read_b128 v[196:199], v217 offset:7168
	global_load_lds_dwordx4 v[200:201], off
	v_lshl_add_u64 v[200:201], s[0:1], 0, v[192:193]
	v_lshl_add_u64 v[200:201], v[200:201], 0, s[22:23]
	s_mov_b32 m0, s62
	s_nop 0
	global_load_lds_dwordx4 v[200:201], off
	s_cmp_lg_u32 s100, 0
	s_waitcnt vmcnt(8)
	s_waitcnt lgkmcnt(0)
	s_barrier
	s_setprio 1
	s_waitcnt lgkmcnt(0)
	s_cbranch_scc1 .Lcz1_579
	v_mfma_f32_16x16x32_bf16 v[122:125], v[130:133], v[162:165], v[122:125]
	v_mfma_f32_16x16x32_bf16 v[126:129], v[138:141], v[162:165], v[126:129]
	v_mfma_f32_16x16x32_bf16 v[110:113], v[130:133], v[170:173], v[110:113]
	v_mfma_f32_16x16x32_bf16 v[106:109], v[138:141], v[170:173], v[106:109]
	v_mfma_f32_16x16x32_bf16 v[94:97], v[130:133], v[178:181], v[94:97]
	v_mfma_f32_16x16x32_bf16 v[90:93], v[138:141], v[178:181], v[90:93]
	v_mfma_f32_16x16x32_bf16 v[78:81], v[130:133], v[186:189], v[78:81]
	v_mfma_f32_16x16x32_bf16 v[74:77], v[138:141], v[186:189], v[74:77]
	v_mfma_f32_16x16x32_bf16 v[122:125], v[134:137], v[166:169], v[122:125]
	v_mfma_f32_16x16x32_bf16 v[126:129], v[142:145], v[166:169], v[126:129]
	v_mfma_f32_16x16x32_bf16 v[110:113], v[134:137], v[174:177], v[110:113]
	v_mfma_f32_16x16x32_bf16 v[106:109], v[142:145], v[174:177], v[106:109]
	v_mfma_f32_16x16x32_bf16 v[94:97], v[134:137], v[182:185], v[94:97]
	v_mfma_f32_16x16x32_bf16 v[90:93], v[142:145], v[182:185], v[90:93]
	v_mfma_f32_16x16x32_bf16 v[78:81], v[134:137], v[196:199], v[78:81]
	v_mfma_f32_16x16x32_bf16 v[74:77], v[142:145], v[196:199], v[74:77]
	v_mfma_f32_16x16x32_bf16 v[118:121], v[146:149], v[162:165], v[118:121]
	v_mfma_f32_16x16x32_bf16 v[114:117], v[154:157], v[162:165], v[114:117]
	v_mfma_f32_16x16x32_bf16 v[102:105], v[146:149], v[170:173], v[102:105]
	v_mfma_f32_16x16x32_bf16 v[98:101], v[154:157], v[170:173], v[98:101]
	v_mfma_f32_16x16x32_bf16 v[86:89], v[146:149], v[178:181], v[86:89]
	v_mfma_f32_16x16x32_bf16 v[82:85], v[154:157], v[178:181], v[82:85]
	v_mfma_f32_16x16x32_bf16 v[70:73], v[146:149], v[186:189], v[70:73]
	v_mfma_f32_16x16x32_bf16 v[66:69], v[154:157], v[186:189], v[66:69]
	v_mfma_f32_16x16x32_bf16 v[118:121], v[150:153], v[166:169], v[118:121]
	v_mfma_f32_16x16x32_bf16 v[114:117], v[158:161], v[166:169], v[114:117]
	v_mfma_f32_16x16x32_bf16 v[102:105], v[150:153], v[174:177], v[102:105]
	v_mfma_f32_16x16x32_bf16 v[98:101], v[158:161], v[174:177], v[98:101]
	v_mfma_f32_16x16x32_bf16 v[86:89], v[150:153], v[182:185], v[86:89]
	v_mfma_f32_16x16x32_bf16 v[82:85], v[158:161], v[182:185], v[82:85]
	v_mfma_f32_16x16x32_bf16 v[70:73], v[150:153], v[196:199], v[70:73]
	v_mfma_f32_16x16x32_bf16 v[66:69], v[158:161], v[196:199], v[66:69]
.Lcj1_579:
	s_setprio 0
	s_barrier
	s_and_b64 s[72:73], s[68:69], exec
	s_cselect_b32 s62, 0, s66
	s_and_b64 s[68:69], s[4:5], s[68:69]
	s_and_b64 s[68:69], s[68:69], exec
	s_cselect_b32 s7, s19, s7
	s_cselect_b32 s6, s18, s6
	s_cselect_b32 s1, s17, s1
	s_cselect_b32 s0, s16, s0
	s_lshl_b64 s[68:69], s[62:63], 7
	s_add_u32 s72, s6, s68
	s_addc_u32 s73, s7, s69
	s_mov_b32 m0, s37
	s_add_u32 s61, s6, 0x60000
	ds_read_b128 v[162:165], v217 offset:16384
	ds_read_b128 v[166:169], v217 offset:17408
	ds_read_b128 v[170:173], v217 offset:18432
	ds_read_b128 v[174:177], v217 offset:19456
	ds_read_b128 v[178:181], v217 offset:20480
	ds_read_b128 v[182:185], v217 offset:21504
	ds_read_b128 v[186:189], v217 offset:22528
	ds_read_b128 v[196:199], v217 offset:23552
	global_load_lds_dwordx4 v190, s[72:73]
	s_mov_b32 m0, s38
	s_addc_u32 s67, s7, 0
	global_load_lds_dwordx4 v216, s[72:73]
	s_add_u32 s72, s61, s68
	s_addc_u32 s73, s67, s69
	s_mov_b32 m0, s39
	s_add_u32 s68, s0, s68
	global_load_lds_dwordx4 v190, s[72:73]
	s_mov_b32 m0, s40
	s_addc_u32 s69, s1, s69
	global_load_lds_dwordx4 v216, s[72:73]
	s_mov_b32 m0, s31
	s_nop 0
	global_load_lds_dwordx4 v194, s[68:69]
	s_mov_b32 m0, s41
	s_nop 0
	global_load_lds_dwordx4 v192, s[68:69]
	s_cmp_lg_u32 s100, 0
	s_waitcnt vmcnt(8)
	s_waitcnt lgkmcnt(0)
	s_barrier
	s_setprio 1
	s_waitcnt lgkmcnt(0)
	s_cbranch_scc1 .Lcz2_579
	v_mfma_f32_16x16x32_bf16 v[62:65], v[130:133], v[162:165], v[62:65]
	v_mfma_f32_16x16x32_bf16 v[58:61], v[138:141], v[162:165], v[58:61]
	v_mfma_f32_16x16x32_bf16 v[46:49], v[130:133], v[170:173], v[46:49]
	v_mfma_f32_16x16x32_bf16 v[42:45], v[138:141], v[170:173], v[42:45]
	v_mfma_f32_16x16x32_bf16 v[30:33], v[130:133], v[178:181], v[30:33]
	v_mfma_f32_16x16x32_bf16 v[26:29], v[138:141], v[178:181], v[26:29]
	v_mfma_f32_16x16x32_bf16 v[14:17], v[130:133], v[186:189], v[14:17]
	v_mfma_f32_16x16x32_bf16 v[10:13], v[138:141], v[186:189], v[10:13]
	v_mfma_f32_16x16x32_bf16 v[62:65], v[134:137], v[166:169], v[62:65]
	v_mfma_f32_16x16x32_bf16 v[58:61], v[142:145], v[166:169], v[58:61]
	v_mfma_f32_16x16x32_bf16 v[46:49], v[134:137], v[174:177], v[46:49]
	v_mfma_f32_16x16x32_bf16 v[42:45], v[142:145], v[174:177], v[42:45]
	v_mfma_f32_16x16x32_bf16 v[30:33], v[134:137], v[182:185], v[30:33]
	v_mfma_f32_16x16x32_bf16 v[26:29], v[142:145], v[182:185], v[26:29]
	v_mfma_f32_16x16x32_bf16 v[14:17], v[134:137], v[196:199], v[14:17]
	v_mfma_f32_16x16x32_bf16 v[10:13], v[142:145], v[196:199], v[10:13]
	v_mfma_f32_16x16x32_bf16 v[54:57], v[146:149], v[162:165], v[54:57]
	v_mfma_f32_16x16x32_bf16 v[50:53], v[154:157], v[162:165], v[50:53]
	v_mfma_f32_16x16x32_bf16 v[38:41], v[146:149], v[170:173], v[38:41]
	v_mfma_f32_16x16x32_bf16 v[34:37], v[154:157], v[170:173], v[34:37]
	v_mfma_f32_16x16x32_bf16 v[22:25], v[146:149], v[178:181], v[22:25]
	v_mfma_f32_16x16x32_bf16 v[18:21], v[154:157], v[178:181], v[18:21]
	v_mfma_f32_16x16x32_bf16 v[6:9], v[146:149], v[186:189], v[6:9]
	v_mfma_f32_16x16x32_bf16 v[2:5], v[154:157], v[186:189], v[2:5]
	v_mfma_f32_16x16x32_bf16 v[54:57], v[150:153], v[166:169], v[54:57]
	v_mfma_f32_16x16x32_bf16 v[50:53], v[158:161], v[166:169], v[50:53]
	v_mfma_f32_16x16x32_bf16 v[38:41], v[150:153], v[174:177], v[38:41]
	v_mfma_f32_16x16x32_bf16 v[34:37], v[158:161], v[174:177], v[34:37]
	v_mfma_f32_16x16x32_bf16 v[22:25], v[150:153], v[182:185], v[22:25]
	v_mfma_f32_16x16x32_bf16 v[18:21], v[158:161], v[182:185], v[18:21]
	v_mfma_f32_16x16x32_bf16 v[6:9], v[150:153], v[196:199], v[6:9]
	v_mfma_f32_16x16x32_bf16 v[2:5], v[158:161], v[196:199], v[2:5]
.Lcj2_579:
	s_setprio 0
	s_barrier
	v_add_u32_e32 v142, 0x18000, v191
	v_add_u32_e32 v158, 0x1c000, v191
	ds_read_b128 v[130:133], v142
	ds_read_b128 v[134:137], v142 offset:1024
	ds_read_b128 v[138:141], v142 offset:2048
	ds_read_b128 v[142:145], v142 offset:3072
	ds_read_b128 v[146:149], v158
	ds_read_b128 v[150:153], v158 offset:1024
	ds_read_b128 v[154:157], v158 offset:2048
	ds_read_b128 v[158:161], v158 offset:3072
	s_add_u32 s68, s68, 0x60000
	s_addc_u32 s69, s69, 0
	s_mov_b32 m0, s42
	ds_read_b128 v[162:165], v217 offset:32768
	ds_read_b128 v[166:169], v217 offset:33792
	ds_read_b128 v[170:173], v217 offset:34816
	ds_read_b128 v[174:177], v217 offset:35840
	ds_read_b128 v[178:181], v217 offset:36864
	ds_read_b128 v[182:185], v217 offset:37888
	ds_read_b128 v[186:189], v217 offset:38912
	ds_read_b128 v[196:199], v217 offset:39936
	global_load_lds_dwordx4 v194, s[68:69]
	s_mov_b32 m0, s43
	s_nop 0
	global_load_lds_dwordx4 v192, s[68:69]
	s_waitcnt vmcnt(8)
	s_waitcnt lgkmcnt(0)
	s_barrier
	s_setprio 1
	s_waitcnt lgkmcnt(0)
	v_mfma_f32_16x16x32_bf16 v[122:125], v[130:133], v[162:165], v[122:125]
	v_mfma_f32_16x16x32_bf16 v[126:129], v[138:141], v[162:165], v[126:129]
	v_mfma_f32_16x16x32_bf16 v[110:113], v[130:133], v[170:173], v[110:113]
	v_mfma_f32_16x16x32_bf16 v[106:109], v[138:141], v[170:173], v[106:109]
	v_mfma_f32_16x16x32_bf16 v[94:97], v[130:133], v[178:181], v[94:97]
	v_mfma_f32_16x16x32_bf16 v[90:93], v[138:141], v[178:181], v[90:93]
	v_mfma_f32_16x16x32_bf16 v[78:81], v[130:133], v[186:189], v[78:81]
	v_mfma_f32_16x16x32_bf16 v[74:77], v[138:141], v[186:189], v[74:77]
	v_mfma_f32_16x16x32_bf16 v[122:125], v[134:137], v[166:169], v[122:125]
	v_mfma_f32_16x16x32_bf16 v[126:129], v[142:145], v[166:169], v[126:129]
	v_mfma_f32_16x16x32_bf16 v[110:113], v[134:137], v[174:177], v[110:113]
	v_mfma_f32_16x16x32_bf16 v[106:109], v[142:145], v[174:177], v[106:109]
	v_mfma_f32_16x16x32_bf16 v[94:97], v[134:137], v[182:185], v[94:97]
	v_mfma_f32_16x16x32_bf16 v[90:93], v[142:145], v[182:185], v[90:93]
	v_mfma_f32_16x16x32_bf16 v[78:81], v[134:137], v[196:199], v[78:81]
	v_mfma_f32_16x16x32_bf16 v[74:77], v[142:145], v[196:199], v[74:77]
	v_mfma_f32_16x16x32_bf16 v[118:121], v[146:149], v[162:165], v[118:121]
	v_mfma_f32_16x16x32_bf16 v[114:117], v[154:157], v[162:165], v[114:117]
	v_mfma_f32_16x16x32_bf16 v[102:105], v[146:149], v[170:173], v[102:105]
	v_mfma_f32_16x16x32_bf16 v[98:101], v[154:157], v[170:173], v[98:101]
	v_mfma_f32_16x16x32_bf16 v[86:89], v[146:149], v[178:181], v[86:89]
	v_mfma_f32_16x16x32_bf16 v[82:85], v[154:157], v[178:181], v[82:85]
	v_mfma_f32_16x16x32_bf16 v[70:73], v[146:149], v[186:189], v[70:73]
	v_mfma_f32_16x16x32_bf16 v[66:69], v[154:157], v[186:189], v[66:69]
	v_mfma_f32_16x16x32_bf16 v[118:121], v[150:153], v[166:169], v[118:121]
	v_mfma_f32_16x16x32_bf16 v[114:117], v[158:161], v[166:169], v[114:117]
	v_mfma_f32_16x16x32_bf16 v[102:105], v[150:153], v[174:177], v[102:105]
	v_mfma_f32_16x16x32_bf16 v[98:101], v[158:161], v[174:177], v[98:101]
	v_mfma_f32_16x16x32_bf16 v[86:89], v[150:153], v[182:185], v[86:89]
	v_mfma_f32_16x16x32_bf16 v[82:85], v[158:161], v[182:185], v[82:85]
	v_mfma_f32_16x16x32_bf16 v[70:73], v[150:153], v[196:199], v[70:73]
	v_mfma_f32_16x16x32_bf16 v[66:69], v[158:161], v[196:199], v[66:69]
	s_setprio 0
	s_barrier
	s_or_b32 s62, s62, 1
	s_lshl_b64 s[68:69], s[62:63], 7
	s_add_u32 s72, s6, s68
	s_mov_b32 m0, s46
	s_addc_u32 s73, s7, s69
	ds_read_b128 v[162:165], v217 offset:49152
	ds_read_b128 v[166:169], v217 offset:50176
	ds_read_b128 v[170:173], v217 offset:51200
	ds_read_b128 v[174:177], v217 offset:52224
	ds_read_b128 v[178:181], v217 offset:53248
	ds_read_b128 v[182:185], v217 offset:54272
	ds_read_b128 v[186:189], v217 offset:55296
	ds_read_b128 v[196:199], v217 offset:56320
	global_load_lds_dwordx4 v190, s[72:73]
	s_mov_b32 m0, s47
	s_nop 0
	global_load_lds_dwordx4 v216, s[72:73]
	s_add_u32 s72, s61, s68
	s_addc_u32 s73, s67, s69
	s_mov_b32 m0, s50
	s_add_u32 s68, s0, s68
	global_load_lds_dwordx4 v190, s[72:73]
	s_mov_b32 m0, s51
	s_addc_u32 s69, s1, s69
	global_load_lds_dwordx4 v216, s[72:73]
	s_mov_b32 m0, s48
	s_nop 0
	global_load_lds_dwordx4 v194, s[68:69]
	s_mov_b32 m0, s49
	s_nop 0
	global_load_lds_dwordx4 v192, s[68:69]
	s_waitcnt vmcnt(8)
	s_waitcnt lgkmcnt(0)
	s_barrier
	s_setprio 1
	s_waitcnt lgkmcnt(0)
	v_mfma_f32_16x16x32_bf16 v[62:65], v[130:133], v[162:165], v[62:65]
	v_mfma_f32_16x16x32_bf16 v[58:61], v[138:141], v[162:165], v[58:61]
	v_mfma_f32_16x16x32_bf16 v[46:49], v[130:133], v[170:173], v[46:49]
	v_mfma_f32_16x16x32_bf16 v[42:45], v[138:141], v[170:173], v[42:45]
	v_mfma_f32_16x16x32_bf16 v[30:33], v[130:133], v[178:181], v[30:33]
	v_mfma_f32_16x16x32_bf16 v[26:29], v[138:141], v[178:181], v[26:29]
	v_mfma_f32_16x16x32_bf16 v[14:17], v[130:133], v[186:189], v[14:17]
	v_mfma_f32_16x16x32_bf16 v[10:13], v[138:141], v[186:189], v[10:13]
	v_mfma_f32_16x16x32_bf16 v[62:65], v[134:137], v[166:169], v[62:65]
	v_mfma_f32_16x16x32_bf16 v[58:61], v[142:145], v[166:169], v[58:61]
	v_mfma_f32_16x16x32_bf16 v[46:49], v[134:137], v[174:177], v[46:49]
	v_mfma_f32_16x16x32_bf16 v[42:45], v[142:145], v[174:177], v[42:45]
	v_mfma_f32_16x16x32_bf16 v[30:33], v[134:137], v[182:185], v[30:33]
	v_mfma_f32_16x16x32_bf16 v[26:29], v[142:145], v[182:185], v[26:29]
	v_mfma_f32_16x16x32_bf16 v[14:17], v[134:137], v[196:199], v[14:17]
	v_mfma_f32_16x16x32_bf16 v[10:13], v[142:145], v[196:199], v[10:13]
	v_mfma_f32_16x16x32_bf16 v[54:57], v[146:149], v[162:165], v[54:57]
	v_mfma_f32_16x16x32_bf16 v[50:53], v[154:157], v[162:165], v[50:53]
	v_mfma_f32_16x16x32_bf16 v[38:41], v[146:149], v[170:173], v[38:41]
	v_mfma_f32_16x16x32_bf16 v[34:37], v[154:157], v[170:173], v[34:37]
	v_mfma_f32_16x16x32_bf16 v[22:25], v[146:149], v[178:181], v[22:25]
	v_mfma_f32_16x16x32_bf16 v[18:21], v[154:157], v[178:181], v[18:21]
	v_mfma_f32_16x16x32_bf16 v[6:9], v[146:149], v[186:189], v[6:9]
	v_mfma_f32_16x16x32_bf16 v[2:5], v[154:157], v[186:189], v[2:5]
	v_mfma_f32_16x16x32_bf16 v[54:57], v[150:153], v[166:169], v[54:57]
	v_mfma_f32_16x16x32_bf16 v[50:53], v[158:161], v[166:169], v[50:53]
	v_mfma_f32_16x16x32_bf16 v[38:41], v[150:153], v[174:177], v[38:41]
	v_mfma_f32_16x16x32_bf16 v[34:37], v[158:161], v[174:177], v[34:37]
	v_mfma_f32_16x16x32_bf16 v[22:25], v[150:153], v[182:185], v[22:25]
	v_mfma_f32_16x16x32_bf16 v[18:21], v[158:161], v[182:185], v[18:21]
	v_mfma_f32_16x16x32_bf16 v[6:9], v[150:153], v[196:199], v[6:9]
	v_mfma_f32_16x16x32_bf16 v[2:5], v[158:161], v[196:199], v[2:5]
	s_setprio 0
	s_barrier
	s_add_u32 s22, s22, 0x100
	s_addc_u32 s23, s23, 0
	s_cmp_ge_i32 s66, s58
	s_cbranch_scc1 .LBB0_583
	s_mov_b32 s61, s66
	s_mov_b32 s73, 0x10000
	s_branch .LBB0_579
.Lcz1_579:
	v_mfma_f32_16x16x32_bf16 v[122:125], v[130:133], v[162:165], 0
	v_mfma_f32_16x16x32_bf16 v[126:129], v[138:141], v[162:165], 0
	v_mfma_f32_16x16x32_bf16 v[110:113], v[130:133], v[170:173], 0
	v_mfma_f32_16x16x32_bf16 v[106:109], v[138:141], v[170:173], 0
	v_mfma_f32_16x16x32_bf16 v[94:97], v[130:133], v[178:181], 0
	v_mfma_f32_16x16x32_bf16 v[90:93], v[138:141], v[178:181], 0
	v_mfma_f32_16x16x32_bf16 v[78:81], v[130:133], v[186:189], 0
	v_mfma_f32_16x16x32_bf16 v[74:77], v[138:141], v[186:189], 0
	v_mfma_f32_16x16x32_bf16 v[122:125], v[134:137], v[166:169], v[122:125]
	v_mfma_f32_16x16x32_bf16 v[126:129], v[142:145], v[166:169], v[126:129]
	v_mfma_f32_16x16x32_bf16 v[110:113], v[134:137], v[174:177], v[110:113]
	v_mfma_f32_16x16x32_bf16 v[106:109], v[142:145], v[174:177], v[106:109]
	v_mfma_f32_16x16x32_bf16 v[94:97], v[134:137], v[182:185], v[94:97]
	v_mfma_f32_16x16x32_bf16 v[90:93], v[142:145], v[182:185], v[90:93]
	v_mfma_f32_16x16x32_bf16 v[78:81], v[134:137], v[196:199], v[78:81]
	v_mfma_f32_16x16x32_bf16 v[74:77], v[142:145], v[196:199], v[74:77]
	v_mfma_f32_16x16x32_bf16 v[118:121], v[146:149], v[162:165], 0
	v_mfma_f32_16x16x32_bf16 v[114:117], v[154:157], v[162:165], 0
	v_mfma_f32_16x16x32_bf16 v[102:105], v[146:149], v[170:173], 0
	v_mfma_f32_16x16x32_bf16 v[98:101], v[154:157], v[170:173], 0
	v_mfma_f32_16x16x32_bf16 v[86:89], v[146:149], v[178:181], 0
	v_mfma_f32_16x16x32_bf16 v[82:85], v[154:157], v[178:181], 0
	v_mfma_f32_16x16x32_bf16 v[70:73], v[146:149], v[186:189], 0
	v_mfma_f32_16x16x32_bf16 v[66:69], v[154:157], v[186:189], 0
	v_mfma_f32_16x16x32_bf16 v[118:121], v[150:153], v[166:169], v[118:121]
	v_mfma_f32_16x16x32_bf16 v[114:117], v[158:161], v[166:169], v[114:117]
	v_mfma_f32_16x16x32_bf16 v[102:105], v[150:153], v[174:177], v[102:105]
	v_mfma_f32_16x16x32_bf16 v[98:101], v[158:161], v[174:177], v[98:101]
	v_mfma_f32_16x16x32_bf16 v[86:89], v[150:153], v[182:185], v[86:89]
	v_mfma_f32_16x16x32_bf16 v[82:85], v[158:161], v[182:185], v[82:85]
	v_mfma_f32_16x16x32_bf16 v[70:73], v[150:153], v[196:199], v[70:73]
	v_mfma_f32_16x16x32_bf16 v[66:69], v[158:161], v[196:199], v[66:69]
	s_branch .Lcj1_579
.Lcz2_579:
	v_mfma_f32_16x16x32_bf16 v[62:65], v[130:133], v[162:165], 0
	v_mfma_f32_16x16x32_bf16 v[58:61], v[138:141], v[162:165], 0
	v_mfma_f32_16x16x32_bf16 v[46:49], v[130:133], v[170:173], 0
	v_mfma_f32_16x16x32_bf16 v[42:45], v[138:141], v[170:173], 0
	v_mfma_f32_16x16x32_bf16 v[30:33], v[130:133], v[178:181], 0
	v_mfma_f32_16x16x32_bf16 v[26:29], v[138:141], v[178:181], 0
	v_mfma_f32_16x16x32_bf16 v[14:17], v[130:133], v[186:189], 0
	v_mfma_f32_16x16x32_bf16 v[10:13], v[138:141], v[186:189], 0
	v_mfma_f32_16x16x32_bf16 v[62:65], v[134:137], v[166:169], v[62:65]
	v_mfma_f32_16x16x32_bf16 v[58:61], v[142:145], v[166:169], v[58:61]
	v_mfma_f32_16x16x32_bf16 v[46:49], v[134:137], v[174:177], v[46:49]
	v_mfma_f32_16x16x32_bf16 v[42:45], v[142:145], v[174:177], v[42:45]
	v_mfma_f32_16x16x32_bf16 v[30:33], v[134:137], v[182:185], v[30:33]
	v_mfma_f32_16x16x32_bf16 v[26:29], v[142:145], v[182:185], v[26:29]
	v_mfma_f32_16x16x32_bf16 v[14:17], v[134:137], v[196:199], v[14:17]
	v_mfma_f32_16x16x32_bf16 v[10:13], v[142:145], v[196:199], v[10:13]
	v_mfma_f32_16x16x32_bf16 v[54:57], v[146:149], v[162:165], 0
	v_mfma_f32_16x16x32_bf16 v[50:53], v[154:157], v[162:165], 0
	v_mfma_f32_16x16x32_bf16 v[38:41], v[146:149], v[170:173], 0
	v_mfma_f32_16x16x32_bf16 v[34:37], v[154:157], v[170:173], 0
	v_mfma_f32_16x16x32_bf16 v[22:25], v[146:149], v[178:181], 0
	v_mfma_f32_16x16x32_bf16 v[18:21], v[154:157], v[178:181], 0
	v_mfma_f32_16x16x32_bf16 v[6:9], v[146:149], v[186:189], 0
	v_mfma_f32_16x16x32_bf16 v[2:5], v[154:157], v[186:189], 0
	v_mfma_f32_16x16x32_bf16 v[54:57], v[150:153], v[166:169], v[54:57]
	v_mfma_f32_16x16x32_bf16 v[50:53], v[158:161], v[166:169], v[50:53]
	v_mfma_f32_16x16x32_bf16 v[38:41], v[150:153], v[174:177], v[38:41]
	v_mfma_f32_16x16x32_bf16 v[34:37], v[158:161], v[174:177], v[34:37]
	v_mfma_f32_16x16x32_bf16 v[22:25], v[150:153], v[182:185], v[22:25]
	v_mfma_f32_16x16x32_bf16 v[18:21], v[158:161], v[182:185], v[18:21]
	v_mfma_f32_16x16x32_bf16 v[6:9], v[150:153], v[196:199], v[6:9]
	v_mfma_f32_16x16x32_bf16 v[2:5], v[158:161], v[196:199], v[2:5]
	s_mov_b32 s100, 0
	s_branch .Lcj2_579

.LBB0_662:
	v_add_u32_e32 v142, 0x10000, v191
	v_add_u32_e32 v158, 0x14000, v191
	ds_read_b128 v[130:133], v142
	ds_read_b128 v[134:137], v142 offset:1024
	ds_read_b128 v[138:141], v142 offset:2048
	ds_read_b128 v[142:145], v142 offset:3072
	ds_read_b128 v[146:149], v158
	ds_read_b128 v[150:153], v158 offset:1024
	ds_read_b128 v[154:157], v158 offset:2048
	ds_read_b128 v[158:161], v158 offset:3072
	s_add_i32 m0, s31, 0xc000
	s_add_i32 s58, s31, 0xe000
	s_cmp_eq_u32 s52, s55
	s_cselect_b64 s[56:57], -1, 0
	v_lshl_add_u64 v[200:201], s[0:1], 0, v[194:195]
	v_lshl_add_u64 v[200:201], v[200:201], 0, s[22:23]
	v_mov_b32_e32 v193, v195
	ds_read_b128 v[162:165], v217
	ds_read_b128 v[166:169], v217 offset:1024
	ds_read_b128 v[170:173], v217 offset:2048
	ds_read_b128 v[174:177], v217 offset:3072
	ds_read_b128 v[178:181], v217 offset:4096
	ds_read_b128 v[182:185], v217 offset:5120
	ds_read_b128 v[186:189], v217 offset:6144
	ds_read_b128 v[196:199], v217 offset:7168
	global_load_lds_dwordx4 v[200:201], off
	v_lshl_add_u64 v[200:201], s[0:1], 0, v[192:193]
	v_lshl_add_u64 v[200:201], v[200:201], 0, s[22:23]
	s_mov_b32 m0, s58
	s_nop 0
	global_load_lds_dwordx4 v[200:201], off
	s_cmp_lg_u32 s100, 0
	s_waitcnt vmcnt(8)
	s_waitcnt lgkmcnt(0)
	s_barrier
	s_setprio 1
	s_waitcnt lgkmcnt(0)
	s_cbranch_scc1 .Lcz1_662
	v_mfma_f32_16x16x32_bf16 v[126:129], v[130:133], v[162:165], v[126:129]
	v_mfma_f32_16x16x32_bf16 v[122:125], v[138:141], v[162:165], v[122:125]
	v_mfma_f32_16x16x32_bf16 v[110:113], v[130:133], v[170:173], v[110:113]
	v_mfma_f32_16x16x32_bf16 v[106:109], v[138:141], v[170:173], v[106:109]
	v_mfma_f32_16x16x32_bf16 v[94:97], v[130:133], v[178:181], v[94:97]
	v_mfma_f32_16x16x32_bf16 v[90:93], v[138:141], v[178:181], v[90:93]
	v_mfma_f32_16x16x32_bf16 v[78:81], v[130:133], v[186:189], v[78:81]
	v_mfma_f32_16x16x32_bf16 v[74:77], v[138:141], v[186:189], v[74:77]
	v_mfma_f32_16x16x32_bf16 v[126:129], v[134:137], v[166:169], v[126:129]
	v_mfma_f32_16x16x32_bf16 v[122:125], v[142:145], v[166:169], v[122:125]
	v_mfma_f32_16x16x32_bf16 v[110:113], v[134:137], v[174:177], v[110:113]
	v_mfma_f32_16x16x32_bf16 v[106:109], v[142:145], v[174:177], v[106:109]
	v_mfma_f32_16x16x32_bf16 v[94:97], v[134:137], v[182:185], v[94:97]
	v_mfma_f32_16x16x32_bf16 v[90:93], v[142:145], v[182:185], v[90:93]
	v_mfma_f32_16x16x32_bf16 v[78:81], v[134:137], v[196:199], v[78:81]
	v_mfma_f32_16x16x32_bf16 v[74:77], v[142:145], v[196:199], v[74:77]
	v_mfma_f32_16x16x32_bf16 v[118:121], v[146:149], v[162:165], v[118:121]
	v_mfma_f32_16x16x32_bf16 v[114:117], v[154:157], v[162:165], v[114:117]
	v_mfma_f32_16x16x32_bf16 v[102:105], v[146:149], v[170:173], v[102:105]
	v_mfma_f32_16x16x32_bf16 v[98:101], v[154:157], v[170:173], v[98:101]
	v_mfma_f32_16x16x32_bf16 v[86:89], v[146:149], v[178:181], v[86:89]
	v_mfma_f32_16x16x32_bf16 v[82:85], v[154:157], v[178:181], v[82:85]
	v_mfma_f32_16x16x32_bf16 v[70:73], v[146:149], v[186:189], v[70:73]
	v_mfma_f32_16x16x32_bf16 v[66:69], v[154:157], v[186:189], v[66:69]
	v_mfma_f32_16x16x32_bf16 v[118:121], v[150:153], v[166:169], v[118:121]
	v_mfma_f32_16x16x32_bf16 v[114:117], v[158:161], v[166:169], v[114:117]
	v_mfma_f32_16x16x32_bf16 v[102:105], v[150:153], v[174:177], v[102:105]
	v_mfma_f32_16x16x32_bf16 v[98:101], v[158:161], v[174:177], v[98:101]
	v_mfma_f32_16x16x32_bf16 v[86:89], v[150:153], v[182:185], v[86:89]
	v_mfma_f32_16x16x32_bf16 v[82:85], v[158:161], v[182:185], v[82:85]
	v_mfma_f32_16x16x32_bf16 v[70:73], v[150:153], v[196:199], v[70:73]
	v_mfma_f32_16x16x32_bf16 v[66:69], v[158:161], v[196:199], v[66:69]
.Lcj1_662:
	s_setprio 0
	s_barrier
	s_and_b64 s[58:59], s[56:57], exec
	s_cselect_b32 s62, 0, s55
	s_and_b64 s[56:57], s[2:3], s[56:57]
	s_and_b64 s[56:57], s[56:57], exec
	s_cselect_b32 s5, s54, s5
	s_cselect_b32 s4, s17, s4
	s_cselect_b32 s1, s53, s1
	s_cselect_b32 s0, s19, s0
	s_lshl_b64 s[56:57], s[62:63], 7
	s_add_u32 s58, s4, s56
	s_addc_u32 s59, s5, s57
	s_mov_b32 m0, s37
	s_add_u32 s60, s4, 0x40000
	ds_read_b128 v[162:165], v217 offset:16384
	ds_read_b128 v[166:169], v217 offset:17408
	ds_read_b128 v[170:173], v217 offset:18432
	ds_read_b128 v[174:177], v217 offset:19456
	ds_read_b128 v[178:181], v217 offset:20480
	ds_read_b128 v[182:185], v217 offset:21504
	ds_read_b128 v[186:189], v217 offset:22528
	ds_read_b128 v[196:199], v217 offset:23552
	global_load_lds_dwordx4 v190, s[58:59]
	s_mov_b32 m0, s38
	s_addc_u32 s61, s5, 0
	global_load_lds_dwordx4 v216, s[58:59]
	s_add_u32 s58, s60, s56
	s_addc_u32 s59, s61, s57
	s_mov_b32 m0, s39
	s_add_u32 s56, s0, s56
	global_load_lds_dwordx4 v190, s[58:59]
	s_mov_b32 m0, s40
	s_addc_u32 s57, s1, s57
	global_load_lds_dwordx4 v216, s[58:59]
	s_mov_b32 m0, s31
	s_nop 0
	global_load_lds_dwordx4 v194, s[56:57]
	s_mov_b32 m0, s41
	s_nop 0
	global_load_lds_dwordx4 v192, s[56:57]
	s_cmp_lg_u32 s100, 0
	s_waitcnt vmcnt(8)
	s_waitcnt lgkmcnt(0)
	s_barrier
	s_setprio 1
	s_waitcnt lgkmcnt(0)
	s_cbranch_scc1 .Lcz2_662
	v_mfma_f32_16x16x32_bf16 v[62:65], v[130:133], v[162:165], v[62:65]
	v_mfma_f32_16x16x32_bf16 v[58:61], v[138:141], v[162:165], v[58:61]
	v_mfma_f32_16x16x32_bf16 v[46:49], v[130:133], v[170:173], v[46:49]
	v_mfma_f32_16x16x32_bf16 v[42:45], v[138:141], v[170:173], v[42:45]
	v_mfma_f32_16x16x32_bf16 v[30:33], v[130:133], v[178:181], v[30:33]
	v_mfma_f32_16x16x32_bf16 v[26:29], v[138:141], v[178:181], v[26:29]
	v_mfma_f32_16x16x32_bf16 v[14:17], v[130:133], v[186:189], v[14:17]
	v_mfma_f32_16x16x32_bf16 v[10:13], v[138:141], v[186:189], v[10:13]
	v_mfma_f32_16x16x32_bf16 v[62:65], v[134:137], v[166:169], v[62:65]
	v_mfma_f32_16x16x32_bf16 v[58:61], v[142:145], v[166:169], v[58:61]
	v_mfma_f32_16x16x32_bf16 v[46:49], v[134:137], v[174:177], v[46:49]
	v_mfma_f32_16x16x32_bf16 v[42:45], v[142:145], v[174:177], v[42:45]
	v_mfma_f32_16x16x32_bf16 v[30:33], v[134:137], v[182:185], v[30:33]
	v_mfma_f32_16x16x32_bf16 v[26:29], v[142:145], v[182:185], v[26:29]
	v_mfma_f32_16x16x32_bf16 v[14:17], v[134:137], v[196:199], v[14:17]
	v_mfma_f32_16x16x32_bf16 v[10:13], v[142:145], v[196:199], v[10:13]
	v_mfma_f32_16x16x32_bf16 v[54:57], v[146:149], v[162:165], v[54:57]
	v_mfma_f32_16x16x32_bf16 v[50:53], v[154:157], v[162:165], v[50:53]
	v_mfma_f32_16x16x32_bf16 v[38:41], v[146:149], v[170:173], v[38:41]
	v_mfma_f32_16x16x32_bf16 v[34:37], v[154:157], v[170:173], v[34:37]
	v_mfma_f32_16x16x32_bf16 v[22:25], v[146:149], v[178:181], v[22:25]
	v_mfma_f32_16x16x32_bf16 v[18:21], v[154:157], v[178:181], v[18:21]
	v_mfma_f32_16x16x32_bf16 v[6:9], v[146:149], v[186:189], v[6:9]
	v_mfma_f32_16x16x32_bf16 v[2:5], v[154:157], v[186:189], v[2:5]
	v_mfma_f32_16x16x32_bf16 v[54:57], v[150:153], v[166:169], v[54:57]
	v_mfma_f32_16x16x32_bf16 v[50:53], v[158:161], v[166:169], v[50:53]
	v_mfma_f32_16x16x32_bf16 v[38:41], v[150:153], v[174:177], v[38:41]
	v_mfma_f32_16x16x32_bf16 v[34:37], v[158:161], v[174:177], v[34:37]
	v_mfma_f32_16x16x32_bf16 v[22:25], v[150:153], v[182:185], v[22:25]
	v_mfma_f32_16x16x32_bf16 v[18:21], v[158:161], v[182:185], v[18:21]
	v_mfma_f32_16x16x32_bf16 v[6:9], v[150:153], v[196:199], v[6:9]
	v_mfma_f32_16x16x32_bf16 v[2:5], v[158:161], v[196:199], v[2:5]
.Lcj2_662:
	s_setprio 0
	s_barrier
	v_add_u32_e32 v142, 0x18000, v191
	v_add_u32_e32 v158, 0x1c000, v191
	ds_read_b128 v[130:133], v142
	ds_read_b128 v[134:137], v142 offset:1024
	ds_read_b128 v[138:141], v142 offset:2048
	ds_read_b128 v[142:145], v142 offset:3072
	ds_read_b128 v[146:149], v158
	ds_read_b128 v[150:153], v158 offset:1024
	ds_read_b128 v[154:157], v158 offset:2048
	ds_read_b128 v[158:161], v158 offset:3072
	s_add_u32 s56, s56, 0x40000
	s_addc_u32 s57, s57, 0
	s_mov_b32 m0, s42
	ds_read_b128 v[162:165], v217 offset:32768
	ds_read_b128 v[166:169], v217 offset:33792
	ds_read_b128 v[170:173], v217 offset:34816
	ds_read_b128 v[174:177], v217 offset:35840
	ds_read_b128 v[178:181], v217 offset:36864
	ds_read_b128 v[182:185], v217 offset:37888
	ds_read_b128 v[186:189], v217 offset:38912
	ds_read_b128 v[196:199], v217 offset:39936
	global_load_lds_dwordx4 v194, s[56:57]
	s_mov_b32 m0, s43
	s_nop 0
	global_load_lds_dwordx4 v192, s[56:57]
	s_waitcnt vmcnt(8)
	s_waitcnt lgkmcnt(0)
	s_barrier
	s_setprio 1
	s_waitcnt lgkmcnt(0)
	v_mfma_f32_16x16x32_bf16 v[126:129], v[130:133], v[162:165], v[126:129]
	v_mfma_f32_16x16x32_bf16 v[122:125], v[138:141], v[162:165], v[122:125]
	v_mfma_f32_16x16x32_bf16 v[110:113], v[130:133], v[170:173], v[110:113]
	v_mfma_f32_16x16x32_bf16 v[106:109], v[138:141], v[170:173], v[106:109]
	v_mfma_f32_16x16x32_bf16 v[94:97], v[130:133], v[178:181], v[94:97]
	v_mfma_f32_16x16x32_bf16 v[90:93], v[138:141], v[178:181], v[90:93]
	v_mfma_f32_16x16x32_bf16 v[78:81], v[130:133], v[186:189], v[78:81]
	v_mfma_f32_16x16x32_bf16 v[74:77], v[138:141], v[186:189], v[74:77]
	v_mfma_f32_16x16x32_bf16 v[126:129], v[134:137], v[166:169], v[126:129]
	v_mfma_f32_16x16x32_bf16 v[122:125], v[142:145], v[166:169], v[122:125]
	v_mfma_f32_16x16x32_bf16 v[110:113], v[134:137], v[174:177], v[110:113]
	v_mfma_f32_16x16x32_bf16 v[106:109], v[142:145], v[174:177], v[106:109]
	v_mfma_f32_16x16x32_bf16 v[94:97], v[134:137], v[182:185], v[94:97]
	v_mfma_f32_16x16x32_bf16 v[90:93], v[142:145], v[182:185], v[90:93]
	v_mfma_f32_16x16x32_bf16 v[78:81], v[134:137], v[196:199], v[78:81]
	v_mfma_f32_16x16x32_bf16 v[74:77], v[142:145], v[196:199], v[74:77]
	v_mfma_f32_16x16x32_bf16 v[118:121], v[146:149], v[162:165], v[118:121]
	v_mfma_f32_16x16x32_bf16 v[114:117], v[154:157], v[162:165], v[114:117]
	v_mfma_f32_16x16x32_bf16 v[102:105], v[146:149], v[170:173], v[102:105]
	v_mfma_f32_16x16x32_bf16 v[98:101], v[154:157], v[170:173], v[98:101]
	v_mfma_f32_16x16x32_bf16 v[86:89], v[146:149], v[178:181], v[86:89]
	v_mfma_f32_16x16x32_bf16 v[82:85], v[154:157], v[178:181], v[82:85]
	v_mfma_f32_16x16x32_bf16 v[70:73], v[146:149], v[186:189], v[70:73]
	v_mfma_f32_16x16x32_bf16 v[66:69], v[154:157], v[186:189], v[66:69]
	v_mfma_f32_16x16x32_bf16 v[118:121], v[150:153], v[166:169], v[118:121]
	v_mfma_f32_16x16x32_bf16 v[114:117], v[158:161], v[166:169], v[114:117]
	v_mfma_f32_16x16x32_bf16 v[102:105], v[150:153], v[174:177], v[102:105]
	v_mfma_f32_16x16x32_bf16 v[98:101], v[158:161], v[174:177], v[98:101]
	v_mfma_f32_16x16x32_bf16 v[86:89], v[150:153], v[182:185], v[86:89]
	v_mfma_f32_16x16x32_bf16 v[82:85], v[158:161], v[182:185], v[82:85]
	v_mfma_f32_16x16x32_bf16 v[70:73], v[150:153], v[196:199], v[70:73]
	v_mfma_f32_16x16x32_bf16 v[66:69], v[158:161], v[196:199], v[66:69]
	s_setprio 0
	s_barrier
	s_or_b32 s62, s62, 1
	s_lshl_b64 s[56:57], s[62:63], 7
	s_add_u32 s58, s4, s56
	s_mov_b32 m0, s45
	s_addc_u32 s59, s5, s57
	ds_read_b128 v[162:165], v217 offset:49152
	ds_read_b128 v[166:169], v217 offset:50176
	ds_read_b128 v[170:173], v217 offset:51200
	ds_read_b128 v[174:177], v217 offset:52224
	ds_read_b128 v[178:181], v217 offset:53248
	ds_read_b128 v[182:185], v217 offset:54272
	ds_read_b128 v[186:189], v217 offset:55296
	ds_read_b128 v[196:199], v217 offset:56320
	global_load_lds_dwordx4 v190, s[58:59]
	s_mov_b32 m0, s46
	s_nop 0
	global_load_lds_dwordx4 v216, s[58:59]
	s_add_u32 s58, s60, s56
	s_addc_u32 s59, s61, s57
	s_mov_b32 m0, s49
	s_add_u32 s56, s0, s56
	global_load_lds_dwordx4 v190, s[58:59]
	s_mov_b32 m0, s50
	s_addc_u32 s57, s1, s57
	global_load_lds_dwordx4 v216, s[58:59]
	s_mov_b32 m0, s47
	s_nop 0
	global_load_lds_dwordx4 v194, s[56:57]
	s_mov_b32 m0, s48
	s_nop 0
	global_load_lds_dwordx4 v192, s[56:57]
	s_waitcnt vmcnt(8)
	s_waitcnt lgkmcnt(0)
	s_barrier
	s_setprio 1
	s_waitcnt lgkmcnt(0)
	v_mfma_f32_16x16x32_bf16 v[62:65], v[130:133], v[162:165], v[62:65]
	v_mfma_f32_16x16x32_bf16 v[58:61], v[138:141], v[162:165], v[58:61]
	v_mfma_f32_16x16x32_bf16 v[46:49], v[130:133], v[170:173], v[46:49]
	v_mfma_f32_16x16x32_bf16 v[42:45], v[138:141], v[170:173], v[42:45]
	v_mfma_f32_16x16x32_bf16 v[30:33], v[130:133], v[178:181], v[30:33]
	v_mfma_f32_16x16x32_bf16 v[26:29], v[138:141], v[178:181], v[26:29]
	v_mfma_f32_16x16x32_bf16 v[14:17], v[130:133], v[186:189], v[14:17]
	v_mfma_f32_16x16x32_bf16 v[10:13], v[138:141], v[186:189], v[10:13]
	v_mfma_f32_16x16x32_bf16 v[62:65], v[134:137], v[166:169], v[62:65]
	v_mfma_f32_16x16x32_bf16 v[58:61], v[142:145], v[166:169], v[58:61]
	v_mfma_f32_16x16x32_bf16 v[46:49], v[134:137], v[174:177], v[46:49]
	v_mfma_f32_16x16x32_bf16 v[42:45], v[142:145], v[174:177], v[42:45]
	v_mfma_f32_16x16x32_bf16 v[30:33], v[134:137], v[182:185], v[30:33]
	v_mfma_f32_16x16x32_bf16 v[26:29], v[142:145], v[182:185], v[26:29]
	v_mfma_f32_16x16x32_bf16 v[14:17], v[134:137], v[196:199], v[14:17]
	v_mfma_f32_16x16x32_bf16 v[10:13], v[142:145], v[196:199], v[10:13]
	v_mfma_f32_16x16x32_bf16 v[54:57], v[146:149], v[162:165], v[54:57]
	v_mfma_f32_16x16x32_bf16 v[50:53], v[154:157], v[162:165], v[50:53]
	v_mfma_f32_16x16x32_bf16 v[38:41], v[146:149], v[170:173], v[38:41]
	v_mfma_f32_16x16x32_bf16 v[34:37], v[154:157], v[170:173], v[34:37]
	v_mfma_f32_16x16x32_bf16 v[22:25], v[146:149], v[178:181], v[22:25]
	v_mfma_f32_16x16x32_bf16 v[18:21], v[154:157], v[178:181], v[18:21]
	v_mfma_f32_16x16x32_bf16 v[6:9], v[146:149], v[186:189], v[6:9]
	v_mfma_f32_16x16x32_bf16 v[2:5], v[154:157], v[186:189], v[2:5]
	v_mfma_f32_16x16x32_bf16 v[54:57], v[150:153], v[166:169], v[54:57]
	v_mfma_f32_16x16x32_bf16 v[50:53], v[158:161], v[166:169], v[50:53]
	v_mfma_f32_16x16x32_bf16 v[38:41], v[150:153], v[174:177], v[38:41]
	v_mfma_f32_16x16x32_bf16 v[34:37], v[158:161], v[174:177], v[34:37]
	v_mfma_f32_16x16x32_bf16 v[22:25], v[150:153], v[182:185], v[22:25]
	v_mfma_f32_16x16x32_bf16 v[18:21], v[158:161], v[182:185], v[18:21]
	v_mfma_f32_16x16x32_bf16 v[6:9], v[150:153], v[196:199], v[6:9]
	v_mfma_f32_16x16x32_bf16 v[2:5], v[158:161], v[196:199], v[2:5]
	s_setprio 0
	s_barrier
	s_add_i32 s56, s55, 2
	s_add_u32 s22, s22, 0x100
	s_addc_u32 s23, s23, 0
	s_cmp_ge_i32 s55, s52
	s_mov_b32 s55, s56
	s_cbranch_scc0 .LBB0_662
	s_branch .Lcsk_662
.Lcz1_662:
	v_mfma_f32_16x16x32_bf16 v[126:129], v[130:133], v[162:165], 0
	v_mfma_f32_16x16x32_bf16 v[122:125], v[138:141], v[162:165], 0
	v_mfma_f32_16x16x32_bf16 v[110:113], v[130:133], v[170:173], 0
	v_mfma_f32_16x16x32_bf16 v[106:109], v[138:141], v[170:173], 0
	v_mfma_f32_16x16x32_bf16 v[94:97], v[130:133], v[178:181], 0
	v_mfma_f32_16x16x32_bf16 v[90:93], v[138:141], v[178:181], 0
	v_mfma_f32_16x16x32_bf16 v[78:81], v[130:133], v[186:189], 0
	v_mfma_f32_16x16x32_bf16 v[74:77], v[138:141], v[186:189], 0
	v_mfma_f32_16x16x32_bf16 v[126:129], v[134:137], v[166:169], v[126:129]
	v_mfma_f32_16x16x32_bf16 v[122:125], v[142:145], v[166:169], v[122:125]
	v_mfma_f32_16x16x32_bf16 v[110:113], v[134:137], v[174:177], v[110:113]
	v_mfma_f32_16x16x32_bf16 v[106:109], v[142:145], v[174:177], v[106:109]
	v_mfma_f32_16x16x32_bf16 v[94:97], v[134:137], v[182:185], v[94:97]
	v_mfma_f32_16x16x32_bf16 v[90:93], v[142:145], v[182:185], v[90:93]
	v_mfma_f32_16x16x32_bf16 v[78:81], v[134:137], v[196:199], v[78:81]
	v_mfma_f32_16x16x32_bf16 v[74:77], v[142:145], v[196:199], v[74:77]
	v_mfma_f32_16x16x32_bf16 v[118:121], v[146:149], v[162:165], 0
	v_mfma_f32_16x16x32_bf16 v[114:117], v[154:157], v[162:165], 0
	v_mfma_f32_16x16x32_bf16 v[102:105], v[146:149], v[170:173], 0
	v_mfma_f32_16x16x32_bf16 v[98:101], v[154:157], v[170:173], 0
	v_mfma_f32_16x16x32_bf16 v[86:89], v[146:149], v[178:181], 0
	v_mfma_f32_16x16x32_bf16 v[82:85], v[154:157], v[178:181], 0
	v_mfma_f32_16x16x32_bf16 v[70:73], v[146:149], v[186:189], 0
	v_mfma_f32_16x16x32_bf16 v[66:69], v[154:157], v[186:189], 0
	v_mfma_f32_16x16x32_bf16 v[118:121], v[150:153], v[166:169], v[118:121]
	v_mfma_f32_16x16x32_bf16 v[114:117], v[158:161], v[166:169], v[114:117]
	v_mfma_f32_16x16x32_bf16 v[102:105], v[150:153], v[174:177], v[102:105]
	v_mfma_f32_16x16x32_bf16 v[98:101], v[158:161], v[174:177], v[98:101]
	v_mfma_f32_16x16x32_bf16 v[86:89], v[150:153], v[182:185], v[86:89]
	v_mfma_f32_16x16x32_bf16 v[82:85], v[158:161], v[182:185], v[82:85]
	v_mfma_f32_16x16x32_bf16 v[70:73], v[150:153], v[196:199], v[70:73]
	v_mfma_f32_16x16x32_bf16 v[66:69], v[158:161], v[196:199], v[66:69]
	s_branch .Lcj1_662

.LBB0_961:
	v_add_u32_e32 v2, 0x10000, v167
	v_add_u32_e32 v14, 0x14000, v167
	ds_read_b128 v[18:21], v2
	ds_read_b128 v[22:25], v2 offset:1024
	ds_read_b128 v[26:29], v2 offset:2048
	ds_read_b128 v[30:33], v2 offset:3072
	ds_read_b128 v[2:5], v14
	ds_read_b128 v[6:9], v14 offset:1024
	ds_read_b128 v[10:13], v14 offset:2048
	ds_read_b128 v[14:17], v14 offset:3072
	s_add_i32 m0, s41, 0xc000
	s_add_i32 s28, s41, 0xe000
	s_cmp_lg_u32 s19, s60
	s_cselect_b64 s[30:31], -1, 0
	v_lshl_add_u64 v[188:189], s[20:21], 0, v[194:195]
	v_lshl_add_u64 v[188:189], v[188:189], 0, s[26:27]
	v_mov_b32_e32 v169, v195
	ds_read_b128 v[180:183], v170
	ds_read_b128 v[184:187], v170 offset:1024
	ds_read_b128 v[216:219], v170 offset:2048
	ds_read_b128 v[220:223], v170 offset:3072
	ds_read_b128 v[224:227], v170 offset:4096
	ds_read_b128 v[228:231], v170 offset:5120
	ds_read_b128 v[196:199], v170 offset:6144
	ds_read_b128 v[200:203], v170 offset:7168
	global_load_lds_dwordx4 v[188:189], off
	v_lshl_add_u64 v[188:189], s[20:21], 0, v[168:169]
	v_lshl_add_u64 v[188:189], v[188:189], 0, s[26:27]
	s_mov_b32 m0, s28
	s_nop 0
	global_load_lds_dwordx4 v[188:189], off
	s_cmp_lg_u32 s100, 0
	s_waitcnt vmcnt(8)
	s_waitcnt lgkmcnt(0)
	s_barrier
	s_setprio 1
	s_waitcnt lgkmcnt(0)
	s_cbranch_scc1 .Lcz1_961
	v_mfma_f32_16x16x128_f8f6f4 v[146:149], v[18:25], v[180:187], v[146:149]
	v_mfma_f32_16x16x128_f8f6f4 v[158:161], v[26:33], v[180:187], v[158:161]
	v_mfma_f32_16x16x128_f8f6f4 v[142:145], v[18:25], v[216:223], v[142:145]
	v_mfma_f32_16x16x128_f8f6f4 v[138:141], v[26:33], v[216:223], v[138:141]
	v_mfma_f32_16x16x128_f8f6f4 v[126:129], v[18:25], v[224:231], v[126:129]
	v_mfma_f32_16x16x128_f8f6f4 v[122:125], v[26:33], v[224:231], v[122:125]
	v_mfma_f32_16x16x128_f8f6f4 v[110:113], v[18:25], v[196:203], v[110:113]
	v_mfma_f32_16x16x128_f8f6f4 v[106:109], v[26:33], v[196:203], v[106:109]
	v_mfma_f32_16x16x128_f8f6f4 v[154:157], v[2:9], v[180:187], v[154:157]
	v_mfma_f32_16x16x128_f8f6f4 v[150:153], v[10:17], v[180:187], v[150:153]
	v_mfma_f32_16x16x128_f8f6f4 v[134:137], v[2:9], v[216:223], v[134:137]
	v_mfma_f32_16x16x128_f8f6f4 v[130:133], v[10:17], v[216:223], v[130:133]
	v_mfma_f32_16x16x128_f8f6f4 v[118:121], v[2:9], v[224:231], v[118:121]
	v_mfma_f32_16x16x128_f8f6f4 v[114:117], v[10:17], v[224:231], v[114:117]
	v_mfma_f32_16x16x128_f8f6f4 v[102:105], v[2:9], v[196:203], v[102:105]
	v_mfma_f32_16x16x128_f8f6f4 v[98:101], v[10:17], v[196:203], v[98:101]

.LBB0_963:
	s_ashr_i32 s29, s28, 31
	s_lshl_b64 s[28:29], s[28:29], 7
	s_add_u32 s30, s12, s28
	s_mov_b32 m0, s42
	s_addc_u32 s31, s13, s29
	ds_read_b128 v[180:183], v170 offset:16384
	ds_read_b128 v[184:187], v170 offset:17408
	ds_read_b128 v[196:199], v170 offset:18432
	ds_read_b128 v[200:203], v170 offset:19456
	ds_read_b128 v[216:219], v170 offset:20480
	ds_read_b128 v[220:223], v170 offset:21504
	ds_read_b128 v[224:227], v170 offset:22528
	ds_read_b128 v[228:231], v170 offset:23552
	global_load_lds_dwordx4 v171, s[30:31]
	s_mov_b32 m0, s43
	s_nop 0
	global_load_lds_dwordx4 v162, s[30:31]
	s_add_u32 s30, s12, 0x20000
	s_addc_u32 s31, s13, 0
	s_add_u32 s66, s30, s28
	s_addc_u32 s67, s31, s29
	s_mov_b32 m0, s44
	s_nop 0
	global_load_lds_dwordx4 v171, s[66:67]
	s_mov_b32 m0, s45
	s_nop 0
	global_load_lds_dwordx4 v162, s[66:67]
	s_add_u32 s66, s20, s28
	s_addc_u32 s67, s21, s29
	s_mov_b32 m0, s41
	s_nop 0
	global_load_lds_dwordx4 v164, s[66:67]
	s_mov_b32 m0, s46
	s_nop 0
	global_load_lds_dwordx4 v166, s[66:67]
	s_cmp_lg_u32 s100, 0
	s_waitcnt vmcnt(8)
	s_waitcnt lgkmcnt(0)
	s_barrier
	s_setprio 1
	s_waitcnt lgkmcnt(0)
	s_cbranch_scc1 .Lcz2_961
	v_mfma_f32_16x16x128_f8f6f4 v[94:97], v[18:25], v[180:187], v[94:97]
	v_mfma_f32_16x16x128_f8f6f4 v[90:93], v[26:33], v[180:187], v[90:93]
	v_mfma_f32_16x16x128_f8f6f4 v[78:81], v[18:25], v[196:203], v[78:81]
	v_mfma_f32_16x16x128_f8f6f4 v[74:77], v[26:33], v[196:203], v[74:77]
	v_mfma_f32_16x16x128_f8f6f4 v[188:191], v[18:25], v[216:223], v[62:65]
	v_mfma_f32_16x16x128_f8f6f4 v[248:251], v[26:33], v[216:223], v[58:61]
	v_mfma_f32_16x16x128_f8f6f4 v[242:245], v[18:25], v[224:231], v[46:49]
	v_mfma_f32_16x16x128_f8f6f4 v[208:211], v[26:33], v[224:231], v[42:45]
	v_mfma_f32_16x16x128_f8f6f4 v[86:89], v[2:9], v[180:187], v[86:89]
	v_mfma_f32_16x16x128_f8f6f4 v[82:85], v[10:17], v[180:187], v[82:85]
	v_mfma_f32_16x16x128_f8f6f4 v[70:73], v[2:9], v[196:203], v[70:73]
	v_mfma_f32_16x16x128_f8f6f4 v[66:69], v[10:17], v[196:203], v[66:69]
	v_mfma_f32_16x16x128_f8f6f4 v[212:215], v[2:9], v[216:223], v[54:57]
	v_mfma_f32_16x16x128_f8f6f4 v[216:219], v[10:17], v[216:223], v[50:53]
	v_mfma_f32_16x16x128_f8f6f4 v[220:223], v[2:9], v[224:231], v[38:41]
	v_mfma_f32_16x16x128_f8f6f4 v[224:227], v[10:17], v[224:231], v[34:37]
.Lcj2_961:
	s_setprio 0
	s_barrier
	v_add_u32_e32 v14, 0x18000, v167
	v_add_u32_e32 v30, 0x1c000, v167
	ds_read_b128 v[2:5], v14
	ds_read_b128 v[6:9], v14 offset:1024
	ds_read_b128 v[10:13], v14 offset:2048
	ds_read_b128 v[14:17], v14 offset:3072
	ds_read_b128 v[18:21], v30
	ds_read_b128 v[22:25], v30 offset:1024
	ds_read_b128 v[26:29], v30 offset:2048
	ds_read_b128 v[30:33], v30 offset:3072
	s_mov_b32 m0, s47
	v_lshl_add_u64 v[180:181], s[66:67], 0, v[194:195]
	ds_read_b128 v[34:37], v170 offset:32768
	ds_read_b128 v[38:41], v170 offset:33792
	ds_read_b128 v[42:45], v170 offset:34816
	ds_read_b128 v[46:49], v170 offset:35840
	ds_read_b128 v[50:53], v170 offset:36864
	ds_read_b128 v[54:57], v170 offset:37888
	ds_read_b128 v[58:61], v170 offset:38912
	ds_read_b128 v[62:65], v170 offset:39936
	global_load_lds_dwordx4 v[180:181], off
	v_lshl_add_u64 v[180:181], s[66:67], 0, v[168:169]
	s_mov_b32 m0, s48
	s_nop 0
	global_load_lds_dwordx4 v[180:181], off
	s_waitcnt vmcnt(8)
	s_waitcnt lgkmcnt(0)
	s_barrier
	s_setprio 1
	s_waitcnt lgkmcnt(0)
	v_mfma_f32_16x16x128_f8f6f4 v[146:149], v[2:9], v[34:41], v[146:149]
	v_mfma_f32_16x16x128_f8f6f4 v[158:161], v[10:17], v[34:41], v[158:161]
	v_mfma_f32_16x16x128_f8f6f4 v[142:145], v[2:9], v[42:49], v[142:145]
	v_mfma_f32_16x16x128_f8f6f4 v[138:141], v[10:17], v[42:49], v[138:141]
	v_mfma_f32_16x16x128_f8f6f4 v[126:129], v[2:9], v[50:57], v[126:129]
	v_mfma_f32_16x16x128_f8f6f4 v[122:125], v[10:17], v[50:57], v[122:125]
	v_mfma_f32_16x16x128_f8f6f4 v[110:113], v[2:9], v[58:65], v[110:113]
	v_mfma_f32_16x16x128_f8f6f4 v[106:109], v[10:17], v[58:65], v[106:109]
	v_mfma_f32_16x16x128_f8f6f4 v[154:157], v[18:25], v[34:41], v[154:157]
	v_mfma_f32_16x16x128_f8f6f4 v[150:153], v[26:33], v[34:41], v[150:153]
	v_mfma_f32_16x16x128_f8f6f4 v[134:137], v[18:25], v[42:49], v[134:137]
	v_mfma_f32_16x16x128_f8f6f4 v[130:133], v[26:33], v[42:49], v[130:133]
	v_mfma_f32_16x16x128_f8f6f4 v[118:121], v[18:25], v[50:57], v[118:121]
	v_mfma_f32_16x16x128_f8f6f4 v[114:117], v[26:33], v[50:57], v[114:117]
	v_mfma_f32_16x16x128_f8f6f4 v[102:105], v[18:25], v[58:65], v[102:105]
	v_mfma_f32_16x16x128_f8f6f4 v[98:101], v[26:33], v[58:65], v[98:101]
	s_setprio 0
	s_barrier
	s_add_u32 s61, s28, 0x80
	s_addc_u32 s62, s29, 0
	s_add_u32 s28, s12, s61
	s_mov_b32 m0, s49
	s_addc_u32 s29, s13, s62
	ds_read_b128 v[34:37], v170 offset:49152
	ds_read_b128 v[38:41], v170 offset:50176
	ds_read_b128 v[50:53], v170 offset:51200
	ds_read_b128 v[54:57], v170 offset:52224
	ds_read_b128 v[180:183], v170 offset:53248
	ds_read_b128 v[184:187], v170 offset:54272
	ds_read_b128 v[196:199], v170 offset:55296
	ds_read_b128 v[200:203], v170 offset:56320
	global_load_lds_dwordx4 v171, s[28:29]
	s_mov_b32 m0, s50
	s_nop 0
	global_load_lds_dwordx4 v162, s[28:29]
	s_add_u32 s28, s30, s61
	s_addc_u32 s29, s31, s62
	s_mov_b32 m0, s53
	s_nop 0
	global_load_lds_dwordx4 v171, s[28:29]
	s_mov_b32 m0, s54
	s_nop 0
	global_load_lds_dwordx4 v162, s[28:29]
	s_add_u32 s28, s20, s61
	s_addc_u32 s29, s21, s62
	s_mov_b32 m0, s51
	s_nop 0
	global_load_lds_dwordx4 v164, s[28:29]
	s_mov_b32 m0, s52
	s_nop 0
	global_load_lds_dwordx4 v166, s[28:29]
	s_waitcnt vmcnt(8)
	s_waitcnt lgkmcnt(0)
	s_barrier
	s_setprio 1
	s_waitcnt lgkmcnt(0)
	v_mfma_f32_16x16x128_f8f6f4 v[94:97], v[2:9], v[34:41], v[94:97]
	v_mfma_f32_16x16x128_f8f6f4 v[90:93], v[10:17], v[34:41], v[90:93]
	v_mfma_f32_16x16x128_f8f6f4 v[78:81], v[2:9], v[50:57], v[78:81]
	v_mfma_f32_16x16x128_f8f6f4 v[74:77], v[10:17], v[50:57], v[74:77]
	v_mfma_f32_16x16x128_f8f6f4 v[62:65], v[2:9], v[180:187], v[188:191]
	v_mfma_f32_16x16x128_f8f6f4 v[58:61], v[10:17], v[180:187], v[248:251]
	v_mfma_f32_16x16x128_f8f6f4 v[46:49], v[2:9], v[196:203], v[242:245]
	v_mfma_f32_16x16x128_f8f6f4 v[42:45], v[10:17], v[196:203], v[208:211]
	v_mfma_f32_16x16x128_f8f6f4 v[86:89], v[18:25], v[34:41], v[86:89]
	v_mfma_f32_16x16x128_f8f6f4 v[82:85], v[26:33], v[34:41], v[82:85]
	v_mfma_f32_16x16x128_f8f6f4 v[70:73], v[18:25], v[50:57], v[70:73]
	v_mfma_f32_16x16x128_f8f6f4 v[66:69], v[26:33], v[50:57], v[66:69]
	v_mfma_f32_16x16x128_f8f6f4 v[54:57], v[18:25], v[180:187], v[212:215]
	v_mfma_f32_16x16x128_f8f6f4 v[50:53], v[26:33], v[180:187], v[216:219]
	v_mfma_f32_16x16x128_f8f6f4 v[38:41], v[18:25], v[196:203], v[220:223]
	v_mfma_f32_16x16x128_f8f6f4 v[34:37], v[26:33], v[196:203], v[224:227]
	s_setprio 0
	s_barrier
	s_add_i32 s28, s60, 2
	s_add_u32 s26, s26, 0x100
	s_addc_u32 s27, s27, 0
	s_cmp_ge_i32 s60, s19
	s_cbranch_scc1 .LBB0_966
	s_mov_b32 s60, s28
	s_branch .LBB0_961
.Lcz1_961:
	v_mfma_f32_16x16x128_f8f6f4 v[146:149], v[18:25], v[180:187], 0
	v_mfma_f32_16x16x128_f8f6f4 v[158:161], v[26:33], v[180:187], 0
	v_mfma_f32_16x16x128_f8f6f4 v[142:145], v[18:25], v[216:223], 0
	v_mfma_f32_16x16x128_f8f6f4 v[138:141], v[26:33], v[216:223], 0
	v_mfma_f32_16x16x128_f8f6f4 v[126:129], v[18:25], v[224:231], 0
	v_mfma_f32_16x16x128_f8f6f4 v[122:125], v[26:33], v[224:231], 0
	v_mfma_f32_16x16x128_f8f6f4 v[110:113], v[18:25], v[196:203], 0
	v_mfma_f32_16x16x128_f8f6f4 v[106:109], v[26:33], v[196:203], 0
	v_mfma_f32_16x16x128_f8f6f4 v[154:157], v[2:9], v[180:187], 0
	v_mfma_f32_16x16x128_f8f6f4 v[150:153], v[10:17], v[180:187], 0
	v_mfma_f32_16x16x128_f8f6f4 v[134:137], v[2:9], v[216:223], 0
	v_mfma_f32_16x16x128_f8f6f4 v[130:133], v[10:17], v[216:223], 0
	v_mfma_f32_16x16x128_f8f6f4 v[118:121], v[2:9], v[224:231], 0
	v_mfma_f32_16x16x128_f8f6f4 v[114:117], v[10:17], v[224:231], 0
	v_mfma_f32_16x16x128_f8f6f4 v[102:105], v[2:9], v[196:203], 0
	v_mfma_f32_16x16x128_f8f6f4 v[98:101], v[10:17], v[196:203], 0
	s_branch .Lcj1_961
.Lcz2_961:
	v_mfma_f32_16x16x128_f8f6f4 v[94:97], v[18:25], v[180:187], 0
	v_mfma_f32_16x16x128_f8f6f4 v[90:93], v[26:33], v[180:187], 0
	v_mfma_f32_16x16x128_f8f6f4 v[78:81], v[18:25], v[196:203], 0
	v_mfma_f32_16x16x128_f8f6f4 v[74:77], v[26:33], v[196:203], 0
	v_mfma_f32_16x16x128_f8f6f4 v[188:191], v[18:25], v[216:223], 0
	v_mfma_f32_16x16x128_f8f6f4 v[248:251], v[26:33], v[216:223], 0
	v_mfma_f32_16x16x128_f8f6f4 v[242:245], v[18:25], v[224:231], 0
	v_mfma_f32_16x16x128_f8f6f4 v[208:211], v[26:33], v[224:231], 0
	v_mfma_f32_16x16x128_f8f6f4 v[86:89], v[2:9], v[180:187], 0
	v_mfma_f32_16x16x128_f8f6f4 v[82:85], v[10:17], v[180:187], 0
	v_mfma_f32_16x16x128_f8f6f4 v[70:73], v[2:9], v[196:203], 0
	v_mfma_f32_16x16x128_f8f6f4 v[66:69], v[10:17], v[196:203], 0
	v_mfma_f32_16x16x128_f8f6f4 v[212:215], v[2:9], v[216:223], 0
	v_mfma_f32_16x16x128_f8f6f4 v[216:219], v[10:17], v[216:223], 0
	v_mfma_f32_16x16x128_f8f6f4 v[220:223], v[2:9], v[224:231], 0
	v_mfma_f32_16x16x128_f8f6f4 v[224:227], v[10:17], v[224:231], 0
	s_mov_b32 s100, 0
	s_branch .Lcj2_961

.LBB0_1048:
	v_add_u32_e32 v66, 0x10000, v131
	ds_read_b128 v[136:139], v66
	ds_read_b128 v[140:143], v66 offset:1024
	ds_read_b128 v[144:147], v66 offset:2048
	ds_read_b128 v[148:151], v66 offset:3072
	v_add_u32_e32 v66, 0x14000, v131
	ds_read_b128 v[152:155], v66
	ds_read_b128 v[156:159], v66 offset:1024
	ds_read_b128 v[160:163], v66 offset:2048
	ds_read_b128 v[164:167], v66 offset:3072
	s_add_i32 m0, s31, 0xc000
	s_add_i32 s57, s31, 0xe000
	s_cmp_eq_u32 s55, s56
	s_cselect_b64 s[22:23], -1, 0
	v_lshl_add_u64 v[66:67], s[0:1], 0, v[194:195]
	v_lshl_add_u64 v[66:67], v[66:67], 0, s[20:21]
	v_mov_b32_e32 v133, v195
	ds_read_b128 v[168:171], v135
	ds_read_b128 v[172:175], v135 offset:1024
	ds_read_b128 v[176:179], v135 offset:2048
	ds_read_b128 v[180:183], v135 offset:3072
	ds_read_b128 v[184:187], v135 offset:4096
	ds_read_b128 v[188:191], v135 offset:5120
	ds_read_b128 v[196:199], v135 offset:6144
	ds_read_b128 v[200:203], v135 offset:7168
	global_load_lds_dwordx4 v[66:67], off
	v_lshl_add_u64 v[66:67], s[0:1], 0, v[132:133]
	v_lshl_add_u64 v[66:67], v[66:67], 0, s[20:21]
	s_mov_b32 m0, s57
	s_nop 0
	global_load_lds_dwordx4 v[66:67], off
	s_cmp_lg_u32 s100, 0
	s_waitcnt vmcnt(8)
	s_waitcnt lgkmcnt(0)
	s_barrier
	s_setprio 1
	s_waitcnt lgkmcnt(0)
	s_cbranch_scc1 .Lcz1_1048
	v_mfma_f32_16x16x128_f8f6f4 v[126:129], v[136:143], v[168:175], v[126:129]
	v_mfma_f32_16x16x128_f8f6f4 v[122:125], v[144:151], v[168:175], v[122:125]
	v_mfma_f32_16x16x128_f8f6f4 v[110:113], v[136:143], v[176:183], v[110:113]
	v_mfma_f32_16x16x128_f8f6f4 v[106:109], v[144:151], v[176:183], v[106:109]
	v_mfma_f32_16x16x128_f8f6f4 v[208:211], v[136:143], v[184:191], v[94:97]
	v_mfma_f32_16x16x128_f8f6f4 v[212:215], v[144:151], v[184:191], v[90:93]
	v_mfma_f32_16x16x128_f8f6f4 v[216:219], v[136:143], v[196:203], v[78:81]
	v_mfma_f32_16x16x128_f8f6f4 v[220:223], v[144:151], v[196:203], v[74:77]
	v_mfma_f32_16x16x128_f8f6f4 v[118:121], v[152:159], v[168:175], v[118:121]
	v_mfma_f32_16x16x128_f8f6f4 v[114:117], v[160:167], v[168:175], v[114:117]
	v_mfma_f32_16x16x128_f8f6f4 v[102:105], v[152:159], v[176:183], v[102:105]
	v_mfma_f32_16x16x128_f8f6f4 v[98:101], v[160:167], v[176:183], v[98:101]
	v_mfma_f32_16x16x128_f8f6f4 v[168:171], v[152:159], v[184:191], v[86:89]
	v_mfma_f32_16x16x128_f8f6f4 v[172:175], v[160:167], v[184:191], v[82:85]
	v_mfma_f32_16x16x128_f8f6f4 v[176:179], v[152:159], v[196:203], v[70:73]
	v_mfma_f32_16x16x128_f8f6f4 v[180:183], v[160:167], v[196:203], v[10:13]
.Lcj1_1048:
	s_setprio 0
	s_barrier
	s_and_b64 s[58:59], s[22:23], exec
	s_cselect_b32 s62, 0, s56
	s_and_b64 s[22:23], s[4:5], s[22:23]
	s_and_b64 s[22:23], s[22:23], exec
	s_cselect_b32 s7, s19, s7
	s_cselect_b32 s6, s18, s6
	s_cselect_b32 s1, s17, s1
	s_cselect_b32 s0, s16, s0
	s_lshl_b64 s[58:59], s[62:63], 7
	s_add_u32 s22, s6, s58
	s_mov_b32 m0, s36
	s_addc_u32 s23, s7, s59
	ds_read_b128 v[66:69], v135 offset:16384
	ds_read_b128 v[70:73], v135 offset:17408
	ds_read_b128 v[74:77], v135 offset:18432
	ds_read_b128 v[78:81], v135 offset:19456
	ds_read_b128 v[82:85], v135 offset:20480
	ds_read_b128 v[86:89], v135 offset:21504
	ds_read_b128 v[90:93], v135 offset:22528
	ds_read_b128 v[94:97], v135 offset:23552
	global_load_lds_dwordx4 v130, s[22:23]
	s_mov_b32 m0, s37
	s_nop 0
	global_load_lds_dwordx4 v134, s[22:23]
	s_add_u32 s22, s6, 0x58000
	s_addc_u32 s23, s7, 0
	s_add_u32 s60, s22, s58
	s_addc_u32 s61, s23, s59
	s_mov_b32 m0, s38
	s_add_u32 s58, s0, s58
	global_load_lds_dwordx4 v130, s[60:61]
	s_mov_b32 m0, s39
	s_addc_u32 s59, s1, s59
	global_load_lds_dwordx4 v134, s[60:61]
	s_mov_b32 m0, s31
	s_nop 0
	global_load_lds_dwordx4 v194, s[58:59]
	s_mov_b32 m0, s40
	s_nop 0
	global_load_lds_dwordx4 v132, s[58:59]
	s_cmp_lg_u32 s100, 0
	s_waitcnt vmcnt(8)
	s_waitcnt lgkmcnt(0)
	s_barrier
	s_setprio 1
	s_waitcnt lgkmcnt(0)
	s_cbranch_scc1 .Lcz2_1048
	v_mfma_f32_16x16x128_f8f6f4 v[62:65], v[136:143], v[66:73], v[62:65]
	v_mfma_f32_16x16x128_f8f6f4 v[58:61], v[144:151], v[66:73], v[58:61]
	v_mfma_f32_16x16x128_f8f6f4 v[228:231], v[144:151], v[90:97], v[228:231]
	v_mfma_f32_16x16x128_f8f6f4 v[184:187], v[136:143], v[74:81], v[46:49]
	v_mfma_f32_16x16x128_f8f6f4 v[188:191], v[144:151], v[74:81], v[42:45]
	v_mfma_f32_16x16x128_f8f6f4 v[196:199], v[136:143], v[82:89], v[30:33]
	v_mfma_f32_16x16x128_f8f6f4 v[200:203], v[144:151], v[82:89], v[26:29]
	v_mfma_f32_16x16x128_f8f6f4 v[224:227], v[136:143], v[90:97], v[14:17]
	v_mfma_f32_16x16x128_f8f6f4 v[54:57], v[152:159], v[66:73], v[54:57]
	v_mfma_f32_16x16x128_f8f6f4 v[50:53], v[160:167], v[66:73], v[50:53]
	v_mfma_f32_16x16x128_f8f6f4 v[242:245], v[152:159], v[74:81], v[38:41]
	v_mfma_f32_16x16x128_f8f6f4 v[248:251], v[160:167], v[74:81], v[34:37]
	v_mfma_f32_16x16x128_f8f6f4 v[232:235], v[152:159], v[82:89], v[22:25]
	v_mfma_f32_16x16x128_f8f6f4 v[238:241], v[160:167], v[82:89], v[18:21]
	v_mfma_f32_16x16x128_f8f6f4 v[204:207], v[152:159], v[90:97], v[6:9]
	v_mfma_f32_16x16x128_f8f6f4 v[66:69], v[160:167], v[90:97], v[2:5]
.Lcj2_1048:
	s_setprio 0
	s_barrier
	v_add_u32_e32 v10, 0x18000, v131
	s_nop 3
	ds_read_b128 v[2:5], v10
	ds_read_b128 v[6:9], v10 offset:1024
	ds_read_b128 v[18:21], v10 offset:2048
	ds_read_b128 v[22:25], v10 offset:3072
	v_add_u32_e32 v10, 0x1c000, v131
	ds_read_b128 v[136:139], v10
	ds_read_b128 v[140:143], v10 offset:1024
	ds_read_b128 v[144:147], v10 offset:2048
	ds_read_b128 v[148:151], v10 offset:3072
	s_add_u32 s58, s58, 0x58000
	s_addc_u32 s59, s59, 0
	s_mov_b32 m0, s41
	ds_read_b128 v[10:13], v135 offset:32768
	ds_read_b128 v[14:17], v135 offset:33792
	ds_read_b128 v[26:29], v135 offset:34816
	ds_read_b128 v[30:33], v135 offset:35840
	ds_read_b128 v[34:37], v135 offset:36864
	ds_read_b128 v[38:41], v135 offset:37888
	ds_read_b128 v[42:45], v135 offset:38912
	ds_read_b128 v[46:49], v135 offset:39936
	global_load_lds_dwordx4 v194, s[58:59]
	s_mov_b32 m0, s42
	s_nop 0
	global_load_lds_dwordx4 v132, s[58:59]
	s_waitcnt vmcnt(8)
	s_waitcnt lgkmcnt(0)
	s_barrier
	s_setprio 1
	s_waitcnt lgkmcnt(0)
	v_mfma_f32_16x16x128_f8f6f4 v[126:129], v[2:9], v[10:17], v[126:129]
	v_mfma_f32_16x16x128_f8f6f4 v[122:125], v[18:25], v[10:17], v[122:125]
	v_mfma_f32_16x16x128_f8f6f4 v[110:113], v[2:9], v[26:33], v[110:113]
	v_mfma_f32_16x16x128_f8f6f4 v[106:109], v[18:25], v[26:33], v[106:109]
	v_mfma_f32_16x16x128_f8f6f4 v[94:97], v[2:9], v[34:41], v[208:211]
	v_mfma_f32_16x16x128_f8f6f4 v[90:93], v[18:25], v[34:41], v[212:215]
	v_mfma_f32_16x16x128_f8f6f4 v[78:81], v[2:9], v[42:49], v[216:219]
	v_mfma_f32_16x16x128_f8f6f4 v[74:77], v[18:25], v[42:49], v[220:223]
	v_mfma_f32_16x16x128_f8f6f4 v[118:121], v[136:143], v[10:17], v[118:121]
	v_mfma_f32_16x16x128_f8f6f4 v[114:117], v[144:151], v[10:17], v[114:117]
	v_mfma_f32_16x16x128_f8f6f4 v[102:105], v[136:143], v[26:33], v[102:105]
	v_mfma_f32_16x16x128_f8f6f4 v[98:101], v[144:151], v[26:33], v[98:101]
	v_mfma_f32_16x16x128_f8f6f4 v[86:89], v[136:143], v[34:41], v[168:171]
	v_mfma_f32_16x16x128_f8f6f4 v[82:85], v[144:151], v[34:41], v[172:175]
	v_mfma_f32_16x16x128_f8f6f4 v[70:73], v[136:143], v[42:49], v[176:179]
	v_mfma_f32_16x16x128_f8f6f4 v[10:13], v[144:151], v[42:49], v[180:183]
	s_setprio 0
	s_barrier
	s_or_b32 s62, s62, 1
	s_lshl_b64 s[58:59], s[62:63], 7
	s_add_u32 s60, s6, s58
	s_mov_b32 m0, s43
	s_addc_u32 s61, s7, s59
	ds_read_b128 v[34:37], v135 offset:49152
	ds_read_b128 v[38:41], v135 offset:50176
	ds_read_b128 v[152:155], v135 offset:51200
	ds_read_b128 v[156:159], v135 offset:52224
	ds_read_b128 v[160:163], v135 offset:53248
	ds_read_b128 v[164:167], v135 offset:54272
	ds_read_b128 v[168:171], v135 offset:55296
	ds_read_b128 v[172:175], v135 offset:56320
	global_load_lds_dwordx4 v130, s[60:61]
	s_mov_b32 m0, s44
	s_add_u32 s22, s22, s58
	global_load_lds_dwordx4 v134, s[60:61]
	s_addc_u32 s23, s23, s59
	s_mov_b32 m0, s47
	s_nop 0
	global_load_lds_dwordx4 v130, s[22:23]
	s_mov_b32 m0, s48
	s_nop 0
	global_load_lds_dwordx4 v134, s[22:23]
	s_add_u32 s22, s0, s58
	s_addc_u32 s23, s1, s59
	s_mov_b32 m0, s45
	s_nop 0
	global_load_lds_dwordx4 v194, s[22:23]
	s_mov_b32 m0, s46
	s_nop 0
	global_load_lds_dwordx4 v132, s[22:23]
	s_waitcnt vmcnt(8)
	s_waitcnt lgkmcnt(0)
	s_barrier
	s_setprio 1
	s_waitcnt lgkmcnt(0)
	v_mfma_f32_16x16x128_f8f6f4 v[62:65], v[2:9], v[34:41], v[62:65]
	v_mfma_f32_16x16x128_f8f6f4 v[58:61], v[18:25], v[34:41], v[58:61]
	v_mfma_f32_16x16x128_f8f6f4 v[46:49], v[2:9], v[152:159], v[184:187]
	v_mfma_f32_16x16x128_f8f6f4 v[42:45], v[18:25], v[152:159], v[188:191]
	v_mfma_f32_16x16x128_f8f6f4 v[30:33], v[2:9], v[160:167], v[196:199]
	v_mfma_f32_16x16x128_f8f6f4 v[26:29], v[18:25], v[160:167], v[200:203]
	v_mfma_f32_16x16x128_f8f6f4 v[14:17], v[2:9], v[168:175], v[224:227]
	v_mfma_f32_16x16x128_f8f6f4 v[228:231], v[18:25], v[168:175], v[228:231]
	v_mfma_f32_16x16x128_f8f6f4 v[54:57], v[136:143], v[34:41], v[54:57]
	v_mfma_f32_16x16x128_f8f6f4 v[50:53], v[144:151], v[34:41], v[50:53]
	v_mfma_f32_16x16x128_f8f6f4 v[38:41], v[136:143], v[152:159], v[242:245]
	v_mfma_f32_16x16x128_f8f6f4 v[34:37], v[144:151], v[152:159], v[248:251]
	v_mfma_f32_16x16x128_f8f6f4 v[22:25], v[136:143], v[160:167], v[232:235]
	v_mfma_f32_16x16x128_f8f6f4 v[18:21], v[144:151], v[160:167], v[238:241]
	v_mfma_f32_16x16x128_f8f6f4 v[6:9], v[136:143], v[168:175], v[204:207]
	v_mfma_f32_16x16x128_f8f6f4 v[2:5], v[144:151], v[168:175], v[66:69]
	s_setprio 0
	s_barrier
	s_add_i32 s22, s56, 2
	s_add_u32 s20, s20, 0x100
	s_addc_u32 s21, s21, 0
	s_cmp_ge_i32 s56, s55
	s_mov_b32 s56, s22
	s_cbranch_scc0 .LBB0_1048
	s_branch .Lcsk_1048
.Lcz1_1048:
	v_mfma_f32_16x16x128_f8f6f4 v[126:129], v[136:143], v[168:175], 0
	v_mfma_f32_16x16x128_f8f6f4 v[122:125], v[144:151], v[168:175], 0
	v_mfma_f32_16x16x128_f8f6f4 v[110:113], v[136:143], v[176:183], 0
	v_mfma_f32_16x16x128_f8f6f4 v[106:109], v[144:151], v[176:183], 0
	v_mfma_f32_16x16x128_f8f6f4 v[208:211], v[136:143], v[184:191], 0
	v_mfma_f32_16x16x128_f8f6f4 v[212:215], v[144:151], v[184:191], 0
	v_mfma_f32_16x16x128_f8f6f4 v[216:219], v[136:143], v[196:203], 0
	v_mfma_f32_16x16x128_f8f6f4 v[220:223], v[144:151], v[196:203], 0
	v_mfma_f32_16x16x128_f8f6f4 v[118:121], v[152:159], v[168:175], 0
	v_mfma_f32_16x16x128_f8f6f4 v[114:117], v[160:167], v[168:175], 0
	v_mfma_f32_16x16x128_f8f6f4 v[102:105], v[152:159], v[176:183], 0
	v_mfma_f32_16x16x128_f8f6f4 v[98:101], v[160:167], v[176:183], 0
	v_mfma_f32_16x16x128_f8f6f4 v[168:171], v[152:159], v[184:191], 0
	v_mfma_f32_16x16x128_f8f6f4 v[172:175], v[160:167], v[184:191], 0
	v_mfma_f32_16x16x128_f8f6f4 v[176:179], v[152:159], v[196:203], 0
	v_mfma_f32_16x16x128_f8f6f4 v[180:183], v[160:167], v[196:203], 0
	s_branch .Lcj1_1048
.Lcz2_1048:
	v_mfma_f32_16x16x128_f8f6f4 v[62:65], v[136:143], v[66:73], 0
	v_mfma_f32_16x16x128_f8f6f4 v[58:61], v[144:151], v[66:73], 0
	v_mfma_f32_16x16x128_f8f6f4 v[228:231], v[144:151], v[90:97], 0
	v_mfma_f32_16x16x128_f8f6f4 v[184:187], v[136:143], v[74:81], 0
	v_mfma_f32_16x16x128_f8f6f4 v[188:191], v[144:151], v[74:81], 0
	v_mfma_f32_16x16x128_f8f6f4 v[196:199], v[136:143], v[82:89], 0
	v_mfma_f32_16x16x128_f8f6f4 v[200:203], v[144:151], v[82:89], 0
	v_mfma_f32_16x16x128_f8f6f4 v[224:227], v[136:143], v[90:97], 0
	v_mfma_f32_16x16x128_f8f6f4 v[54:57], v[152:159], v[66:73], 0
	v_mfma_f32_16x16x128_f8f6f4 v[50:53], v[160:167], v[66:73], 0
	v_mfma_f32_16x16x128_f8f6f4 v[242:245], v[152:159], v[74:81], 0
	v_mfma_f32_16x16x128_f8f6f4 v[248:251], v[160:167], v[74:81], 0
	v_mfma_f32_16x16x128_f8f6f4 v[232:235], v[152:159], v[82:89], 0
	v_mfma_f32_16x16x128_f8f6f4 v[238:241], v[160:167], v[82:89], 0
	v_mfma_f32_16x16x128_f8f6f4 v[204:207], v[152:159], v[90:97], 0
	v_mfma_f32_16x16x128_f8f6f4 v[66:69], v[160:167], v[90:97], 0
	s_mov_b32 s100, 0
	s_branch .Lcj2_1048
